# s10
# speedup vs baseline: 1.0432x; 1.0062x over previous
.LBB1_1:
	s_or_b64 exec, exec, s[0:1]
	s_add_u32 s2, s2, 0x800000
	s_addc_u32 s3, s3, 0
	s_addk_i32 s76, 0x800
	s_add_i32 s77, s77, 8
	s_addk_i32 s78, 0x400
	s_add_i32 s89, s89, 8
	s_cmp_eq_u32 s2, 0x2000000
	s_waitcnt lgkmcnt(0)
	s_cbranch_scc1 .LBB1_27

.LBB1_4:
	v_readfirstlane_b32 s0, v66
	v_add_u32_e32 v67, 0x2000, v66
	v_lshl_add_u64 v[68:69], s[4:5], 0, v[194:195]
	s_mov_b32 m0, s0
	v_readfirstlane_b32 s0, v67
	v_add_u32_e32 v67, 0x4000, v66
	global_load_lds_dwordx4 v[68:69], off
	v_lshl_add_u64 v[70:71], v[68:69], 0, s[58:59]
	s_mov_b32 m0, s0
	v_readfirstlane_b32 s0, v67
	v_add_u32_e32 v67, 0x6000, v66
	global_load_lds_dwordx4 v[70:71], off
	v_lshl_add_u64 v[70:71], v[68:69], 0, s[60:61]
	s_mov_b32 m0, s0
	v_readfirstlane_b32 s0, v67
	global_load_lds_dwordx4 v[70:71], off
	v_lshl_add_u64 v[68:69], v[68:69], 0, s[62:63]
	s_mov_b32 m0, s0
	v_mov_b32_e32 v94, v66
	global_load_lds_dwordx4 v[68:69], off
	s_waitcnt vmcnt(4)
.LBB1_5:
	v_lshlrev_b32_e32 v67, 4, v1
	v_lshrrev_b32_e32 v1, 1, v1
	v_lshrrev_b32_e32 v69, 5, v132
	v_ashrrev_i32_e32 v66, 4, v132
	v_bitop3_b32 v1, v1, v69, 7 bitop3:0x78
	s_add_u32 s22, s24, s2
	v_lshlrev_b32_e32 v68, 7, v66
	v_lshlrev_b32_e32 v1, 4, v1
	v_and_b32_e32 v0, 8, v0
	s_addc_u32 s90, s25, s3
	v_lshl_or_b32 v201, v66, 12, v67
	v_or3_b32 v0, v68, v1, v0
	v_add_u32_e32 v100, 0x10000, v0
	v_cvt_pk_f16_f32 v1, v64, v65
	v_cvt_pk_f16_f32 v0, v62, v63
	v_cvt_pk_f16_f32 v61, v60, v61
	v_cvt_pk_f16_f32 v60, v58, v59
	ds_write2st64_b64 v100, v[0:1], v[60:61] offset1:8
	v_cvt_pk_f16_f32 v1, v56, v57
	v_cvt_pk_f16_f32 v0, v54, v55
	v_cvt_pk_f16_f32 v53, v52, v53
	v_cvt_pk_f16_f32 v52, v50, v51
	ds_write2st64_b64 v100, v[0:1], v[52:53] offset0:16 offset1:24
	v_cvt_pk_f16_f32 v1, v48, v49
	v_cvt_pk_f16_f32 v0, v46, v47
	v_cvt_pk_f16_f32 v45, v44, v45
	v_cvt_pk_f16_f32 v44, v42, v43
	ds_write2st64_b64 v100, v[0:1], v[44:45] offset0:32 offset1:40
	v_cvt_pk_f16_f32 v1, v40, v41
	v_cvt_pk_f16_f32 v0, v38, v39
	v_cvt_pk_f16_f32 v37, v36, v37
	v_cvt_pk_f16_f32 v36, v34, v35
	ds_write2st64_b64 v100, v[0:1], v[36:37] offset0:48 offset1:56
	s_add_u32 s0, s22, 0x200
	s_addc_u32 s1, s90, 0
	s_add_u32 s70, s0, 0x20000
	s_addc_u32 s71, s1, 0
	s_add_u32 s72, s0, 0x40000
	s_addc_u32 s73, s1, 0
	s_add_u32 s92, s0, 0x60000
	s_addc_u32 s93, s1, 0
	s_add_u32 s94, s0, 0x80000
	s_addc_u32 s95, s1, 0
	s_add_u32 s96, s0, 0xa0000
	s_addc_u32 s97, s1, 0
	s_add_u32 s98, s0, 0xc0000
	s_addc_u32 s99, s1, 0
	s_add_u32 s80, s0, 0xe0000
	s_addc_u32 s81, s1, 0
	global_load_dwordx4 v[70:73], v201, s[0:1] nt
	global_load_dwordx4 v[42:45], v201, s[70:71] nt
	global_load_dwordx4 v[46:49], v201, s[72:73] nt
	global_load_dwordx4 v[66:69], v201, s[92:93] nt
	global_load_dwordx4 v[62:65], v201, s[94:95] nt
	global_load_dwordx4 v[58:61], v201, s[96:97] nt
	global_load_dwordx4 v[54:57], v201, s[98:99] nt
	global_load_dwordx4 v[50:53], v201, s[80:81] nt
	s_waitcnt vmcnt(8)
	s_waitcnt lgkmcnt(0)
	s_barrier
	ds_read_b128 v[34:37], v131
	ds_read_b128 v[38:41], v131 offset:2048
	ds_read_b128 v[74:77], v131 offset:4096
	ds_read_b128 v[78:81], v131 offset:6144
	ds_read_b128 v[82:85], v129
	ds_read_b128 v[86:89], v129 offset:2048
	s_add_u32 s70, s22, 0x300
	v_add_u32_e32 v95, 0x8000, v94
	v_lshl_add_u64 v[0:1], s[26:27], 0, v[196:197]
	s_addc_u32 s71, s90, 0
	v_readfirstlane_b32 s0, v95
	s_mov_b32 m0, s0
	v_cvt_pk_f16_f32 v33, v32, v33
	global_load_lds_dwordx4 v[0:1], off
	v_cvt_pk_f16_f32 v32, v30, v31
	ds_write_b64 v100, v[32:33] offset:32768
	global_load_dwordx4 v[30:33], v201, s[70:71] nt
	s_setprio 1
	s_waitcnt lgkmcnt(1)
	v_mfma_f32_16x16x32_f16 v[90:93], v[82:85], v[34:37], 0
	v_mfma_f32_16x16x32_f16 v[102:105], v[82:85], v[38:41], 0
	v_mfma_f32_16x16x32_f16 v[106:109], v[82:85], v[74:77], 0
	v_mfma_f32_16x16x32_f16 v[82:85], v[82:85], v[78:81], 0
	v_mfma_f32_16x16x32_f16 v[110:113], v[86:89], v[34:37], 0
	v_mfma_f32_16x16x32_f16 v[114:117], v[86:89], v[38:41], 0
	v_mfma_f32_16x16x32_f16 v[118:121], v[86:89], v[74:77], 0
	v_mfma_f32_16x16x32_f16 v[86:89], v[86:89], v[78:81], 0
	s_setprio 0
	ds_read_b128 v[122:125], v129 offset:4096
	ds_read_b128 v[134:137], v129 offset:6144
	v_add_u32_e32 v96, 0xa000, v94
	v_lshl_add_u64 v[98:99], v[0:1], 0, s[58:59]
	v_readfirstlane_b32 s1, v96
	s_mov_b32 m0, s1
	v_cvt_pk_f16_f32 v29, v28, v29
	global_load_lds_dwordx4 v[98:99], off
	v_cvt_pk_f16_f32 v28, v26, v27
	ds_write_b64 v100, v[28:29] offset:36864
	s_add_u32 s70, s22, 0x20300
	s_addc_u32 s71, s90, 0
	global_load_dwordx4 v[26:29], v201, s[70:71] nt
	s_setprio 1
	s_waitcnt lgkmcnt(1)
	v_mfma_f32_16x16x32_f16 v[138:141], v[122:125], v[34:37], 0
	v_mfma_f32_16x16x32_f16 v[142:145], v[122:125], v[38:41], 0
	v_mfma_f32_16x16x32_f16 v[146:149], v[122:125], v[74:77], 0
	v_mfma_f32_16x16x32_f16 v[122:125], v[122:125], v[78:81], 0
	v_mfma_f32_16x16x32_f16 v[150:153], v[134:137], v[34:37], 0
	v_mfma_f32_16x16x32_f16 v[154:157], v[134:137], v[38:41], 0
	v_mfma_f32_16x16x32_f16 v[158:161], v[134:137], v[74:77], 0
	v_mfma_f32_16x16x32_f16 v[134:137], v[134:137], v[78:81], 0
	s_setprio 0
	ds_read_b128 v[162:165], v129 offset:8192
	ds_read_b128 v[166:169], v129 offset:10240
	v_add_u32_e32 v97, 0xc000, v94
	v_lshl_add_u64 v[98:99], v[0:1], 0, s[60:61]
	v_readfirstlane_b32 s71, v97
	s_mov_b32 m0, s71
	v_cvt_pk_f16_f32 v25, v24, v25
	global_load_lds_dwordx4 v[98:99], off
	v_cvt_pk_f16_f32 v24, v22, v23
	ds_write_b64 v100, v[24:25] offset:40960
	s_add_u32 s72, s22, 0x40300
	s_addc_u32 s73, s90, 0
	global_load_dwordx4 v[22:25], v201, s[72:73] nt
	s_setprio 1
	s_waitcnt lgkmcnt(1)
	v_mfma_f32_16x16x32_f16 v[170:173], v[162:165], v[34:37], 0
	v_mfma_f32_16x16x32_f16 v[174:177], v[162:165], v[38:41], 0
	v_mfma_f32_16x16x32_f16 v[178:181], v[162:165], v[74:77], 0
	v_mfma_f32_16x16x32_f16 v[162:165], v[162:165], v[78:81], 0
	v_mfma_f32_16x16x32_f16 v[182:185], v[166:169], v[34:37], 0
	v_mfma_f32_16x16x32_f16 v[186:189], v[166:169], v[38:41], 0
	v_mfma_f32_16x16x32_f16 v[190:193], v[166:169], v[74:77], 0
	v_mfma_f32_16x16x32_f16 v[166:169], v[166:169], v[78:81], 0
	s_setprio 0
	ds_read_b128 v[202:205], v129 offset:12288
	ds_read_b128 v[206:209], v129 offset:14336
	v_add_u32_e32 v98, 0xe000, v94
	v_lshl_add_u64 v[0:1], v[0:1], 0, s[62:63]
	v_readfirstlane_b32 s72, v98
	s_mov_b32 m0, s72
	s_nop 0
	global_load_lds_dwordx4 v[0:1], off
	v_cvt_pk_f16_f32 v1, v20, v21
	v_cvt_pk_f16_f32 v0, v18, v19
	ds_write_b64 v100, v[0:1] offset:45056
	s_add_u32 s80, s22, 0x60300
	s_addc_u32 s81, s90, 0
	global_load_dwordx4 v[18:21], v201, s[80:81] nt
	s_setprio 1
	s_waitcnt lgkmcnt(1)
	v_mfma_f32_16x16x32_f16 v[210:213], v[202:205], v[34:37], 0
	v_mfma_f32_16x16x32_f16 v[214:217], v[202:205], v[38:41], 0
	v_mfma_f32_16x16x32_f16 v[218:221], v[202:205], v[74:77], 0
	v_mfma_f32_16x16x32_f16 v[202:205], v[202:205], v[78:81], 0
	v_mfma_f32_16x16x32_f16 v[74:77], v[206:209], v[74:77], 0
	v_mfma_f32_16x16x32_f16 v[78:81], v[206:209], v[78:81], 0
	v_mfma_f32_16x16x32_f16 v[222:225], v[206:209], v[34:37], 0
	v_mfma_f32_16x16x32_f16 v[226:229], v[206:209], v[38:41], 0
	s_setprio 0
	ds_read_b128 v[206:209], v128
	ds_read_b128 v[230:233], v128 offset:2048
	ds_read_b128 v[234:237], v128 offset:4096
	ds_read_b128 v[238:241], v128 offset:6144
	ds_read_b128 v[34:37], v130
	ds_read_b128 v[38:41], v130 offset:2048
	v_cvt_pk_f16_f32 v1, v16, v17
	v_cvt_pk_f16_f32 v0, v14, v15
	ds_write_b64 v100, v[0:1] offset:49152
	s_add_u32 s80, s22, 0x80300
	s_addc_u32 s81, s90, 0
	global_load_dwordx4 v[14:17], v201, s[80:81] nt
	s_setprio 1
	s_waitcnt lgkmcnt(1)
	v_mfma_f32_16x16x32_f16 v[90:93], v[34:37], v[206:209], v[90:93]
	v_mfma_f32_16x16x32_f16 v[102:105], v[34:37], v[230:233], v[102:105]
	v_mfma_f32_16x16x32_f16 v[106:109], v[34:37], v[234:237], v[106:109]
	v_mfma_f32_16x16x32_f16 v[82:85], v[34:37], v[238:241], v[82:85]
	v_mfma_f32_16x16x32_f16 v[110:113], v[38:41], v[206:209], v[110:113]
	v_mfma_f32_16x16x32_f16 v[114:117], v[38:41], v[230:233], v[114:117]
	v_mfma_f32_16x16x32_f16 v[118:121], v[38:41], v[234:237], v[118:121]
	v_mfma_f32_16x16x32_f16 v[86:89], v[38:41], v[238:241], v[86:89]
	s_setprio 0
	ds_read_b128 v[34:37], v130 offset:4096
	ds_read_b128 v[38:41], v130 offset:6144
	v_cvt_pk_f16_f32 v1, v12, v13
	v_cvt_pk_f16_f32 v0, v10, v11
	ds_write_b64 v100, v[0:1] offset:53248
	s_add_u32 s80, s22, 0xa0300
	s_addc_u32 s81, s90, 0
	global_load_dwordx4 v[10:13], v201, s[80:81] nt
	s_setprio 1
	s_waitcnt lgkmcnt(1)
	v_mfma_f32_16x16x32_f16 v[146:149], v[34:37], v[234:237], v[146:149]
	v_mfma_f32_16x16x32_f16 v[122:125], v[34:37], v[238:241], v[122:125]
	v_mfma_f32_16x16x32_f16 v[134:137], v[38:41], v[238:241], v[134:137]
	v_mfma_f32_16x16x32_f16 v[138:141], v[34:37], v[206:209], v[138:141]
	v_mfma_f32_16x16x32_f16 v[142:145], v[34:37], v[230:233], v[142:145]
	v_mfma_f32_16x16x32_f16 v[150:153], v[38:41], v[206:209], v[150:153]
	v_mfma_f32_16x16x32_f16 v[154:157], v[38:41], v[230:233], v[154:157]
	v_mfma_f32_16x16x32_f16 v[158:161], v[38:41], v[234:237], v[158:161]
	s_setprio 0
	ds_read_b128 v[38:41], v130 offset:8192
	ds_read_b128 v[242:245], v130 offset:10240
	v_cvt_pk_f16_f32 v1, v8, v9
	v_cvt_pk_f16_f32 v0, v6, v7
	ds_write_b64 v100, v[0:1] offset:57344
	s_add_u32 s80, s22, 0xc0300
	s_addc_u32 s81, s90, 0
	global_load_dwordx4 v[34:37], v201, s[80:81] nt
	s_setprio 1
	s_waitcnt lgkmcnt(1)
	v_mfma_f32_16x16x32_f16 v[6:9], v[38:41], v[206:209], v[170:173]
	v_mfma_f32_16x16x32_f16 v[170:173], v[38:41], v[230:233], v[174:177]
	v_mfma_f32_16x16x32_f16 v[174:177], v[38:41], v[234:237], v[178:181]
	v_mfma_f32_16x16x32_f16 v[162:165], v[38:41], v[238:241], v[162:165]
	v_mfma_f32_16x16x32_f16 v[178:181], v[242:245], v[206:209], v[182:185]
	v_mfma_f32_16x16x32_f16 v[182:185], v[242:245], v[230:233], v[186:189]
	v_mfma_f32_16x16x32_f16 v[186:189], v[242:245], v[234:237], v[190:193]
	v_mfma_f32_16x16x32_f16 v[166:169], v[242:245], v[238:241], v[166:169]
	s_setprio 0
	s_nop 0
	ds_read_b128 v[190:193], v130 offset:12288
	ds_read_b128 v[242:245], v130 offset:14336
	v_cvt_pk_f16_f32 v1, v4, v5
	v_cvt_pk_f16_f32 v0, v2, v3
	ds_write_b64 v100, v[0:1] offset:61440
	s_add_u32 s80, s22, 0xe0300
	s_addc_u32 s81, s90, 0
	global_load_dwordx4 v[38:41], v201, s[80:81] nt
	s_setprio 1
	s_waitcnt lgkmcnt(1)
	v_mfma_f32_16x16x32_f16 v[78:81], v[242:245], v[238:241], v[78:81]
	v_mfma_f32_16x16x32_f16 v[210:213], v[190:193], v[206:209], v[210:213]
	v_mfma_f32_16x16x32_f16 v[214:217], v[190:193], v[230:233], v[214:217]
	v_mfma_f32_16x16x32_f16 v[218:221], v[190:193], v[234:237], v[218:221]
	v_mfma_f32_16x16x32_f16 v[190:193], v[190:193], v[238:241], v[202:205]
	v_mfma_f32_16x16x32_f16 v[202:205], v[242:245], v[206:209], v[222:225]
	v_mfma_f32_16x16x32_f16 v[206:209], v[242:245], v[230:233], v[226:229]
	v_mfma_f32_16x16x32_f16 v[222:225], v[242:245], v[234:237], v[74:77]
	s_setprio 0
	s_waitcnt vmcnt(4)
	s_waitcnt lgkmcnt(0)
	s_barrier
	ds_read_b128 v[226:229], v131 offset:32768
	ds_read_b128 v[230:233], v131 offset:34816
	ds_read_b128 v[234:237], v131 offset:36864
	ds_read_b128 v[238:241], v131 offset:38912
	ds_read_b128 v[74:77], v129 offset:32768
	ds_read_b128 v[242:245], v129 offset:34816
	s_add_u32 s80, s22, 0x400
	s_addc_u32 s81, s90, 0
	v_lshl_add_u64 v[198:199], s[28:29], 0, v[196:197]
	v_readfirstlane_b32 s70, v94
	s_mov_b32 m0, s70
	v_cvt_pk_f16_f32 v1, v72, v73
	global_load_lds_dwordx4 v[198:199], off
	v_cvt_pk_f16_f32 v0, v70, v71
	ds_write_b64 v100, v[0:1]
	global_load_dwordx4 v[0:3], v201, s[80:81] nt
	s_setprio 1
	s_waitcnt lgkmcnt(1)
	v_mfma_f32_16x16x32_f16 v[70:73], v[74:77], v[226:229], v[90:93]
	v_mfma_f32_16x16x32_f16 v[90:93], v[74:77], v[230:233], v[102:105]
	v_mfma_f32_16x16x32_f16 v[104:107], v[74:77], v[234:237], v[106:109]
	v_mfma_f32_16x16x32_f16 v[82:85], v[74:77], v[238:241], v[82:85]
	v_mfma_f32_16x16x32_f16 v[108:111], v[242:245], v[226:229], v[110:113]
	v_mfma_f32_16x16x32_f16 v[112:115], v[242:245], v[230:233], v[114:117]
	v_mfma_f32_16x16x32_f16 v[116:119], v[242:245], v[234:237], v[118:121]
	v_mfma_f32_16x16x32_f16 v[86:89], v[242:245], v[238:241], v[86:89]
	s_setprio 0
	ds_read_b128 v[74:77], v129 offset:36864
	ds_read_b128 v[242:245], v129 offset:38912
	v_add_u32_e32 v99, 0x2000, v94
	v_lshl_add_u64 v[4:5], v[198:199], 0, s[58:59]
	v_readfirstlane_b32 s73, v99
	s_mov_b32 m0, s73
	s_nop 0
	global_load_lds_dwordx4 v[4:5], off
	v_cvt_pk_f16_f32 v5, v44, v45
	v_cvt_pk_f16_f32 v4, v42, v43
	ds_write_b64 v100, v[4:5] offset:4096
	s_add_u32 s80, s22, 0x20400
	s_addc_u32 s81, s90, 0
	global_load_dwordx4 v[42:45], v201, s[80:81] nt
	s_setprio 1
	s_waitcnt lgkmcnt(1)
	v_mfma_f32_16x16x32_f16 v[146:149], v[74:77], v[234:237], v[146:149]
	v_mfma_f32_16x16x32_f16 v[120:123], v[74:77], v[238:241], v[122:125]
	v_mfma_f32_16x16x32_f16 v[124:127], v[242:245], v[226:229], v[150:153]
	v_mfma_f32_16x16x32_f16 v[134:137], v[242:245], v[238:241], v[134:137]
	v_mfma_f32_16x16x32_f16 v[138:141], v[74:77], v[226:229], v[138:141]
	v_mfma_f32_16x16x32_f16 v[142:145], v[74:77], v[230:233], v[142:145]
	v_mfma_f32_16x16x32_f16 v[150:153], v[242:245], v[230:233], v[154:157]
	v_mfma_f32_16x16x32_f16 v[154:157], v[242:245], v[234:237], v[158:161]
	s_setprio 0
	ds_read_b128 v[74:77], v129 offset:40960
	s_nop 0
	ds_read_b128 v[158:161], v129 offset:43008
	v_add_u32_e32 v101, 0x4000, v94
	v_lshl_add_u64 v[4:5], v[198:199], 0, s[60:61]
	v_readfirstlane_b32 s91, v101
	s_mov_b32 m0, s91
	s_nop 0
	global_load_lds_dwordx4 v[4:5], off
	v_cvt_pk_f16_f32 v5, v48, v49
	v_cvt_pk_f16_f32 v4, v46, v47
	ds_write_b64 v100, v[4:5] offset:8192
	s_add_u32 s80, s22, 0x40400
	s_addc_u32 s81, s90, 0
	global_load_dwordx4 v[46:49], v201, s[80:81] nt
	s_setprio 1
	s_waitcnt lgkmcnt(1)
	v_mfma_f32_16x16x32_f16 v[4:7], v[74:77], v[226:229], v[6:9]
	v_mfma_f32_16x16x32_f16 v[170:173], v[74:77], v[230:233], v[170:173]
	v_mfma_f32_16x16x32_f16 v[174:177], v[74:77], v[234:237], v[174:177]
	v_mfma_f32_16x16x32_f16 v[162:165], v[74:77], v[238:241], v[162:165]
	v_mfma_f32_16x16x32_f16 v[178:181], v[158:161], v[226:229], v[178:181]
	v_mfma_f32_16x16x32_f16 v[182:185], v[158:161], v[230:233], v[182:185]
	v_mfma_f32_16x16x32_f16 v[186:189], v[158:161], v[234:237], v[186:189]
	v_mfma_f32_16x16x32_f16 v[158:161], v[158:161], v[238:241], v[166:169]
	s_setprio 0
	s_nop 1
	ds_read_b128 v[166:169], v129 offset:45056
	ds_read_b128 v[242:245], v129 offset:47104
	v_add_u32_e32 v102, 0x6000, v94
	v_lshl_add_u64 v[8:9], v[198:199], 0, s[62:63]
	v_readfirstlane_b32 s92, v102
	s_mov_b32 m0, s92
	s_nop 0
	global_load_lds_dwordx4 v[8:9], off
	v_cvt_pk_f16_f32 v9, v68, v69
	v_cvt_pk_f16_f32 v8, v66, v67
	ds_write_b64 v100, v[8:9] offset:12288
	s_add_u32 s80, s22, 0x60400
	s_addc_u32 s81, s90, 0
	global_load_dwordx4 v[74:77], v201, s[80:81] nt
	s_setprio 1
	s_waitcnt lgkmcnt(1)
	v_mfma_f32_16x16x32_f16 v[66:69], v[166:169], v[226:229], v[210:213]
	v_mfma_f32_16x16x32_f16 v[210:213], v[166:169], v[230:233], v[214:217]
	v_mfma_f32_16x16x32_f16 v[214:217], v[166:169], v[234:237], v[218:221]
	v_mfma_f32_16x16x32_f16 v[166:169], v[166:169], v[238:241], v[190:193]
	v_mfma_f32_16x16x32_f16 v[190:193], v[242:245], v[226:229], v[202:205]
	v_mfma_f32_16x16x32_f16 v[202:205], v[242:245], v[230:233], v[206:209]
	v_mfma_f32_16x16x32_f16 v[206:209], v[242:245], v[234:237], v[222:225]
	v_mfma_f32_16x16x32_f16 v[218:221], v[242:245], v[238:241], v[78:81]
	s_setprio 0
	s_nop 0
	ds_read_b128 v[222:225], v128 offset:32768
	ds_read_b128 v[226:229], v128 offset:34816
	ds_read_b128 v[230:233], v128 offset:36864
	ds_read_b128 v[234:237], v128 offset:38912
	ds_read_b128 v[238:241], v130 offset:32768
	ds_read_b128 v[242:245], v130 offset:34816
	v_cvt_pk_f16_f32 v9, v64, v65
	v_cvt_pk_f16_f32 v8, v62, v63
	ds_write_b64 v100, v[8:9] offset:16384
	s_add_u32 s80, s22, 0x80400
	s_addc_u32 s81, s90, 0
	global_load_dwordx4 v[78:81], v201, s[80:81] nt
	s_setprio 1
	s_waitcnt lgkmcnt(1)
	v_mfma_f32_16x16x32_f16 v[62:65], v[238:241], v[222:225], v[70:73]
	v_mfma_f32_16x16x32_f16 v[70:73], v[238:241], v[226:229], v[90:93]
	v_mfma_f32_16x16x32_f16 v[104:107], v[238:241], v[230:233], v[104:107]
	v_mfma_f32_16x16x32_f16 v[108:111], v[242:245], v[222:225], v[108:111]
	v_mfma_f32_16x16x32_f16 v[112:115], v[242:245], v[226:229], v[112:115]
	v_mfma_f32_16x16x32_f16 v[116:119], v[242:245], v[230:233], v[116:119]
	v_mfma_f32_16x16x32_f16 v[238:241], v[238:241], v[234:237], v[82:85]
	v_mfma_f32_16x16x32_f16 v[242:245], v[242:245], v[234:237], v[86:89]
	s_setprio 0
	s_nop 1
	ds_read_b128 v[86:89], v130 offset:36864
	ds_read_b128 v[90:93], v130 offset:38912
	v_cvt_pk_f16_f32 v9, v60, v61
	v_cvt_pk_f16_f32 v8, v58, v59
	ds_write_b64 v100, v[8:9] offset:20480
	s_add_u32 s80, s22, 0xa0400
	s_addc_u32 s81, s90, 0
	global_load_dwordx4 v[82:85], v201, s[80:81] nt
	s_setprio 1
	s_waitcnt lgkmcnt(1)
	v_mfma_f32_16x16x32_f16 v[58:61], v[86:89], v[222:225], v[138:141]
	v_mfma_f32_16x16x32_f16 v[138:141], v[86:89], v[226:229], v[142:145]
	v_mfma_f32_16x16x32_f16 v[142:145], v[86:89], v[230:233], v[146:149]
	v_mfma_f32_16x16x32_f16 v[120:123], v[86:89], v[234:237], v[120:123]
	v_mfma_f32_16x16x32_f16 v[124:127], v[90:93], v[222:225], v[124:127]
	v_mfma_f32_16x16x32_f16 v[146:149], v[90:93], v[226:229], v[150:153]
	v_mfma_f32_16x16x32_f16 v[134:137], v[90:93], v[234:237], v[134:137]
	v_mfma_f32_16x16x32_f16 v[150:153], v[90:93], v[230:233], v[154:157]
	s_setprio 0
	ds_read_b128 v[90:93], v130 offset:40960
	s_nop 0
	ds_read_b128 v[154:157], v130 offset:43008
	v_cvt_pk_f16_f32 v9, v56, v57
	v_cvt_pk_f16_f32 v8, v54, v55
	ds_write_b64 v100, v[8:9] offset:24576
	s_add_u32 s80, s22, 0xc0400
	s_addc_u32 s81, s90, 0
	global_load_dwordx4 v[86:89], v201, s[80:81] nt
	s_setprio 1
	s_waitcnt lgkmcnt(1)
	v_mfma_f32_16x16x32_f16 v[246:249], v[90:93], v[222:225], v[4:7]
	v_mfma_f32_16x16x32_f16 v[170:173], v[90:93], v[226:229], v[170:173]
	v_mfma_f32_16x16x32_f16 v[174:177], v[90:93], v[230:233], v[174:177]
	v_mfma_f32_16x16x32_f16 v[162:165], v[90:93], v[234:237], v[162:165]
	v_mfma_f32_16x16x32_f16 v[178:181], v[154:157], v[222:225], v[178:181]
	v_mfma_f32_16x16x32_f16 v[182:185], v[154:157], v[226:229], v[182:185]
	v_mfma_f32_16x16x32_f16 v[186:189], v[154:157], v[230:233], v[186:189]
	v_mfma_f32_16x16x32_f16 v[154:157], v[154:157], v[234:237], v[158:161]
	s_setprio 0
	ds_read_b128 v[4:7], v130 offset:45056
	ds_read_b128 v[54:57], v130 offset:47104
	v_cvt_pk_f16_f32 v9, v52, v53
	v_cvt_pk_f16_f32 v8, v50, v51
	ds_write_b64 v100, v[8:9] offset:28672
	s_add_u32 s80, s22, 0xe0400
	s_addc_u32 s81, s90, 0
	global_load_dwordx4 v[90:93], v201, s[80:81] nt
	s_setprio 1
	s_waitcnt lgkmcnt(1)
	v_mfma_f32_16x16x32_f16 v[66:69], v[4:7], v[222:225], v[66:69]
	v_mfma_f32_16x16x32_f16 v[158:161], v[4:7], v[226:229], v[210:213]
	v_mfma_f32_16x16x32_f16 v[210:213], v[4:7], v[230:233], v[214:217]
	v_mfma_f32_16x16x32_f16 v[166:169], v[4:7], v[234:237], v[166:169]
	v_mfma_f32_16x16x32_f16 v[190:193], v[54:57], v[222:225], v[190:193]
	v_mfma_f32_16x16x32_f16 v[202:205], v[54:57], v[226:229], v[202:205]
	v_mfma_f32_16x16x32_f16 v[206:209], v[54:57], v[230:233], v[206:209]
	v_mfma_f32_16x16x32_f16 v[214:217], v[54:57], v[234:237], v[218:221]
	s_setprio 0
	s_waitcnt vmcnt(4)
	s_waitcnt lgkmcnt(0)
	s_barrier
	s_nop 0
	ds_read_b128 v[218:221], v131
	ds_read_b128 v[222:225], v131 offset:2048
	ds_read_b128 v[226:229], v131 offset:4096
	ds_read_b128 v[230:233], v131 offset:6144
	ds_read_b128 v[50:53], v129
	ds_read_b128 v[54:57], v129 offset:2048
	s_add_u32 s80, s22, 0x500
	v_lshl_add_u64 v[8:9], s[30:31], 0, v[196:197]
	s_addc_u32 s81, s90, 0
	s_mov_b32 m0, s0
	v_cvt_pk_f16_f32 v5, v32, v33
	global_load_lds_dwordx4 v[8:9], off
	v_cvt_pk_f16_f32 v4, v30, v31
	ds_write_b64 v100, v[4:5] offset:32768
	global_load_dwordx4 v[4:7], v201, s[80:81] nt
	s_setprio 1
	s_waitcnt lgkmcnt(1)
	v_mfma_f32_16x16x32_f16 v[30:33], v[50:53], v[218:221], v[62:65]
	v_mfma_f32_16x16x32_f16 v[70:73], v[50:53], v[222:225], v[70:73]
	v_mfma_f32_16x16x32_f16 v[104:107], v[50:53], v[226:229], v[104:107]
	v_mfma_f32_16x16x32_f16 v[108:111], v[54:57], v[218:221], v[108:111]
	v_mfma_f32_16x16x32_f16 v[112:115], v[54:57], v[222:225], v[112:115]
	v_mfma_f32_16x16x32_f16 v[116:119], v[54:57], v[226:229], v[116:119]
	v_mfma_f32_16x16x32_f16 v[234:237], v[50:53], v[230:233], v[238:241]
	v_mfma_f32_16x16x32_f16 v[238:241], v[54:57], v[230:233], v[242:245]
	s_setprio 0
	ds_read_b128 v[54:57], v129 offset:4096
	ds_read_b128 v[62:65], v129 offset:6144
	s_mov_b32 m0, s1
	v_lshl_add_u64 v[50:51], v[8:9], 0, s[58:59]
	global_load_lds_dwordx4 v[50:51], off
	v_cvt_pk_f16_f32 v29, v28, v29
	v_cvt_pk_f16_f32 v28, v26, v27
	ds_write_b64 v100, v[28:29] offset:36864
	s_add_u32 s0, s22, 0x20500
	s_addc_u32 s1, s90, 0
	global_load_dwordx4 v[50:53], v201, s[0:1] nt
	s_setprio 1
	s_waitcnt lgkmcnt(1)
	v_mfma_f32_16x16x32_f16 v[26:29], v[54:57], v[218:221], v[58:61]
	v_mfma_f32_16x16x32_f16 v[120:123], v[54:57], v[230:233], v[120:123]
	v_mfma_f32_16x16x32_f16 v[124:127], v[62:65], v[218:221], v[124:127]
	v_mfma_f32_16x16x32_f16 v[146:149], v[62:65], v[222:225], v[146:149]
	v_mfma_f32_16x16x32_f16 v[134:137], v[62:65], v[230:233], v[134:137]
	v_mfma_f32_16x16x32_f16 v[138:141], v[54:57], v[222:225], v[138:141]
	v_mfma_f32_16x16x32_f16 v[142:145], v[54:57], v[226:229], v[142:145]
	v_mfma_f32_16x16x32_f16 v[150:153], v[62:65], v[226:229], v[150:153]
	s_setprio 0
	ds_read_b128 v[58:61], v129 offset:8192
	ds_read_b128 v[62:65], v129 offset:10240
	s_mov_b32 m0, s71
	v_lshl_add_u64 v[54:55], v[8:9], 0, s[60:61]
	global_load_lds_dwordx4 v[54:55], off
	v_cvt_pk_f16_f32 v25, v24, v25
	v_cvt_pk_f16_f32 v24, v22, v23
	ds_write_b64 v100, v[24:25] offset:40960
	s_add_u32 s0, s22, 0x40500
	s_addc_u32 s1, s90, 0
	global_load_dwordx4 v[54:57], v201, s[0:1] nt
	s_setprio 1
	s_waitcnt lgkmcnt(1)
	v_mfma_f32_16x16x32_f16 v[22:25], v[58:61], v[218:221], v[246:249]
	v_mfma_f32_16x16x32_f16 v[170:173], v[58:61], v[222:225], v[170:173]
	v_mfma_f32_16x16x32_f16 v[174:177], v[58:61], v[226:229], v[174:177]
	v_mfma_f32_16x16x32_f16 v[162:165], v[58:61], v[230:233], v[162:165]
	v_mfma_f32_16x16x32_f16 v[178:181], v[62:65], v[218:221], v[178:181]
	v_mfma_f32_16x16x32_f16 v[182:185], v[62:65], v[222:225], v[182:185]
	v_mfma_f32_16x16x32_f16 v[186:189], v[62:65], v[226:229], v[186:189]
	v_mfma_f32_16x16x32_f16 v[154:157], v[62:65], v[230:233], v[154:157]
	s_setprio 0
	ds_read_b128 v[62:65], v129 offset:12288
	ds_read_b128 v[242:245], v129 offset:14336
	s_mov_b32 m0, s72
	v_lshl_add_u64 v[8:9], v[8:9], 0, s[62:63]
	global_load_lds_dwordx4 v[8:9], off
	v_cvt_pk_f16_f32 v9, v20, v21
	v_cvt_pk_f16_f32 v8, v18, v19
	ds_write_b64 v100, v[8:9] offset:45056
	s_add_u32 s0, s22, 0x60500
	s_addc_u32 s1, s90, 0
	global_load_dwordx4 v[58:61], v201, s[0:1] nt
	s_setprio 1
	s_waitcnt lgkmcnt(1)
	v_mfma_f32_16x16x32_f16 v[18:21], v[62:65], v[218:221], v[66:69]
	v_mfma_f32_16x16x32_f16 v[158:161], v[62:65], v[222:225], v[158:161]
	v_mfma_f32_16x16x32_f16 v[210:213], v[62:65], v[226:229], v[210:213]
	v_mfma_f32_16x16x32_f16 v[166:169], v[62:65], v[230:233], v[166:169]
	v_mfma_f32_16x16x32_f16 v[190:193], v[242:245], v[218:221], v[190:193]
	v_mfma_f32_16x16x32_f16 v[202:205], v[242:245], v[222:225], v[202:205]
	v_mfma_f32_16x16x32_f16 v[206:209], v[242:245], v[226:229], v[206:209]
	v_mfma_f32_16x16x32_f16 v[214:217], v[242:245], v[230:233], v[214:217]
	s_setprio 0
	ds_read_b128 v[218:221], v128
	ds_read_b128 v[222:225], v128 offset:2048
	ds_read_b128 v[226:229], v128 offset:4096
	ds_read_b128 v[230:233], v128 offset:6144
	ds_read_b128 v[66:69], v130
	ds_read_b128 v[242:245], v130 offset:2048
	v_cvt_pk_f16_f32 v9, v16, v17
	v_cvt_pk_f16_f32 v8, v14, v15
	ds_write_b64 v100, v[8:9] offset:49152
	s_add_u32 s0, s22, 0x80500
	s_addc_u32 s1, s90, 0
	global_load_dwordx4 v[62:65], v201, s[0:1] nt
	s_setprio 1
	s_waitcnt lgkmcnt(1)
	v_mfma_f32_16x16x32_f16 v[14:17], v[66:69], v[218:221], v[30:33]
	v_mfma_f32_16x16x32_f16 v[30:33], v[66:69], v[222:225], v[70:73]
	v_mfma_f32_16x16x32_f16 v[104:107], v[66:69], v[226:229], v[104:107]
	v_mfma_f32_16x16x32_f16 v[108:111], v[242:245], v[218:221], v[108:111]
	v_mfma_f32_16x16x32_f16 v[112:115], v[242:245], v[222:225], v[112:115]
	v_mfma_f32_16x16x32_f16 v[116:119], v[242:245], v[226:229], v[116:119]
	v_mfma_f32_16x16x32_f16 v[234:237], v[66:69], v[230:233], v[234:237]
	v_mfma_f32_16x16x32_f16 v[238:241], v[242:245], v[230:233], v[238:241]
	s_setprio 0
	ds_read_b128 v[70:73], v130 offset:4096
	ds_read_b128 v[242:245], v130 offset:6144
	v_cvt_pk_f16_f32 v9, v12, v13
	v_cvt_pk_f16_f32 v8, v10, v11
	ds_write_b64 v100, v[8:9] offset:53248
	s_add_u32 s0, s22, 0xa0500
	s_addc_u32 s1, s90, 0
	global_load_dwordx4 v[66:69], v201, s[0:1] nt
	s_setprio 1
	s_waitcnt lgkmcnt(1)
	v_mfma_f32_16x16x32_f16 v[26:29], v[70:73], v[218:221], v[26:29]
	v_mfma_f32_16x16x32_f16 v[120:123], v[70:73], v[230:233], v[120:123]
	v_mfma_f32_16x16x32_f16 v[124:127], v[242:245], v[218:221], v[124:127]
	v_mfma_f32_16x16x32_f16 v[146:149], v[242:245], v[222:225], v[146:149]
	v_mfma_f32_16x16x32_f16 v[134:137], v[242:245], v[230:233], v[134:137]
	v_mfma_f32_16x16x32_f16 v[138:141], v[70:73], v[222:225], v[138:141]
	v_mfma_f32_16x16x32_f16 v[142:145], v[70:73], v[226:229], v[142:145]
	v_mfma_f32_16x16x32_f16 v[150:153], v[242:245], v[226:229], v[150:153]
	s_setprio 0
	ds_read_b128 v[8:11], v130 offset:8192
	ds_read_b128 v[242:245], v130 offset:10240
	v_cvt_pk_f16_f32 v13, v36, v37
	v_cvt_pk_f16_f32 v12, v34, v35
	ds_write_b64 v100, v[12:13] offset:57344
	s_add_u32 s0, s22, 0xc0500
	s_addc_u32 s1, s90, 0
	global_load_dwordx4 v[70:73], v201, s[0:1] nt
	s_setprio 1
	s_waitcnt lgkmcnt(1)
	v_mfma_f32_16x16x32_f16 v[22:25], v[8:11], v[218:221], v[22:25]
	v_mfma_f32_16x16x32_f16 v[170:173], v[8:11], v[222:225], v[170:173]
	v_mfma_f32_16x16x32_f16 v[174:177], v[8:11], v[226:229], v[174:177]
	v_mfma_f32_16x16x32_f16 v[162:165], v[8:11], v[230:233], v[162:165]
	v_mfma_f32_16x16x32_f16 v[178:181], v[242:245], v[218:221], v[178:181]
	v_mfma_f32_16x16x32_f16 v[182:185], v[242:245], v[222:225], v[182:185]
	v_mfma_f32_16x16x32_f16 v[186:189], v[242:245], v[226:229], v[186:189]
	v_mfma_f32_16x16x32_f16 v[154:157], v[242:245], v[230:233], v[154:157]
	s_setprio 0
	ds_read_b128 v[8:11], v130 offset:12288
	ds_read_b128 v[242:245], v130 offset:14336
	v_cvt_pk_f16_f32 v13, v40, v41
	v_cvt_pk_f16_f32 v12, v38, v39
	ds_write_b64 v100, v[12:13] offset:61440
	s_add_u32 s0, s22, 0xe0500
	s_addc_u32 s1, s90, 0
	global_load_dwordx4 v[36:39], v201, s[0:1] nt
	s_setprio 1
	s_waitcnt lgkmcnt(1)
	v_mfma_f32_16x16x32_f16 v[246:249], v[8:11], v[218:221], v[18:21]
	v_mfma_f32_16x16x32_f16 v[158:161], v[8:11], v[222:225], v[158:161]
	v_mfma_f32_16x16x32_f16 v[210:213], v[8:11], v[226:229], v[210:213]
	v_mfma_f32_16x16x32_f16 v[166:169], v[8:11], v[230:233], v[166:169]
	v_mfma_f32_16x16x32_f16 v[190:193], v[242:245], v[218:221], v[190:193]
	v_mfma_f32_16x16x32_f16 v[202:205], v[242:245], v[222:225], v[202:205]
	v_mfma_f32_16x16x32_f16 v[206:209], v[242:245], v[226:229], v[206:209]
	v_mfma_f32_16x16x32_f16 v[214:217], v[242:245], v[230:233], v[214:217]
	s_setprio 0
	s_waitcnt vmcnt(4)
	s_waitcnt lgkmcnt(0)
	s_barrier
	ds_read_b128 v[218:221], v131 offset:32768
	ds_read_b128 v[222:225], v131 offset:34816
	ds_read_b128 v[226:229], v131 offset:36864
	ds_read_b128 v[230:233], v131 offset:38912
	ds_read_b128 v[8:11], v129 offset:32768
	ds_read_b128 v[18:21], v129 offset:34816
	s_add_u32 s0, s22, 0x600
	s_addc_u32 s1, s90, 0
	v_lshl_add_u64 v[34:35], s[34:35], 0, v[196:197]
	s_mov_b32 m0, s70
	v_cvt_pk_f16_f32 v3, v2, v3
	global_load_lds_dwordx4 v[34:35], off
	v_cvt_pk_f16_f32 v2, v0, v1
	ds_write_b64 v100, v[2:3]
	global_load_dwordx4 v[0:3], v201, s[0:1] nt
	s_setprio 1
	s_waitcnt lgkmcnt(1)
	v_mfma_f32_16x16x32_f16 v[30:33], v[8:11], v[222:225], v[30:33]
	v_mfma_f32_16x16x32_f16 v[104:107], v[8:11], v[226:229], v[104:107]
	v_mfma_f32_16x16x32_f16 v[108:111], v[18:21], v[218:221], v[108:111]
	v_mfma_f32_16x16x32_f16 v[112:115], v[18:21], v[222:225], v[112:115]
	v_mfma_f32_16x16x32_f16 v[116:119], v[18:21], v[226:229], v[116:119]
	v_mfma_f32_16x16x32_f16 v[242:245], v[8:11], v[218:221], v[14:17]
	v_mfma_f32_16x16x32_f16 v[234:237], v[8:11], v[230:233], v[234:237]
	v_mfma_f32_16x16x32_f16 v[238:241], v[18:21], v[230:233], v[238:241]
	s_setprio 0
	ds_read_b128 v[12:15], v129 offset:36864
	ds_read_b128 v[16:19], v129 offset:38912
	s_mov_b32 m0, s73
	v_lshl_add_u64 v[8:9], v[34:35], 0, s[58:59]
	global_load_lds_dwordx4 v[8:9], off
	v_cvt_pk_f16_f32 v9, v44, v45
	v_cvt_pk_f16_f32 v8, v42, v43
	ds_write_b64 v100, v[8:9] offset:4096
	s_add_u32 s0, s22, 0x20600
	s_addc_u32 s1, s90, 0
	global_load_dwordx4 v[8:11], v201, s[0:1] nt
	s_setprio 1
	s_waitcnt lgkmcnt(1)
	v_mfma_f32_16x16x32_f16 v[40:43], v[12:15], v[218:221], v[26:29]
	v_mfma_f32_16x16x32_f16 v[120:123], v[12:15], v[230:233], v[120:123]
	v_mfma_f32_16x16x32_f16 v[124:127], v[16:19], v[218:221], v[124:127]
	v_mfma_f32_16x16x32_f16 v[146:149], v[16:19], v[222:225], v[146:149]
	v_mfma_f32_16x16x32_f16 v[134:137], v[16:19], v[230:233], v[134:137]
	v_mfma_f32_16x16x32_f16 v[138:141], v[12:15], v[222:225], v[138:141]
	v_mfma_f32_16x16x32_f16 v[142:145], v[12:15], v[226:229], v[142:145]
	v_mfma_f32_16x16x32_f16 v[150:153], v[16:19], v[226:229], v[150:153]
	s_setprio 0
	ds_read_b128 v[16:19], v129 offset:40960
	ds_read_b128 v[26:29], v129 offset:43008
	s_mov_b32 m0, s91
	v_lshl_add_u64 v[12:13], v[34:35], 0, s[60:61]
	global_load_lds_dwordx4 v[12:13], off
	v_cvt_pk_f16_f32 v13, v48, v49
	v_cvt_pk_f16_f32 v12, v46, v47
	ds_write_b64 v100, v[12:13] offset:8192
	s_add_u32 s0, s22, 0x40600
	s_addc_u32 s1, s90, 0
	global_load_dwordx4 v[12:15], v201, s[0:1] nt
	s_setprio 1
	s_waitcnt lgkmcnt(1)
	v_mfma_f32_16x16x32_f16 v[44:47], v[16:19], v[218:221], v[22:25]
	v_mfma_f32_16x16x32_f16 v[170:173], v[16:19], v[222:225], v[170:173]
	v_mfma_f32_16x16x32_f16 v[174:177], v[16:19], v[226:229], v[174:177]
	v_mfma_f32_16x16x32_f16 v[162:165], v[16:19], v[230:233], v[162:165]
	v_mfma_f32_16x16x32_f16 v[178:181], v[26:29], v[218:221], v[178:181]
	v_mfma_f32_16x16x32_f16 v[182:185], v[26:29], v[222:225], v[182:185]
	v_mfma_f32_16x16x32_f16 v[186:189], v[26:29], v[226:229], v[186:189]
	v_mfma_f32_16x16x32_f16 v[154:157], v[26:29], v[230:233], v[154:157]
	s_setprio 0
	ds_read_b128 v[20:23], v129 offset:45056
	ds_read_b128 v[24:27], v129 offset:47104
	s_mov_b32 m0, s92
	v_lshl_add_u64 v[16:17], v[34:35], 0, s[62:63]
	global_load_lds_dwordx4 v[16:17], off
	v_cvt_pk_f16_f32 v17, v76, v77
	v_cvt_pk_f16_f32 v16, v74, v75
	ds_write_b64 v100, v[16:17] offset:12288
	s_add_u32 s0, s22, 0x60600
	s_addc_u32 s1, s90, 0
	global_load_dwordx4 v[16:19], v201, s[0:1] nt
	s_setprio 1
	s_waitcnt lgkmcnt(1)
	v_mfma_f32_16x16x32_f16 v[74:77], v[20:23], v[218:221], v[246:249]
	v_mfma_f32_16x16x32_f16 v[158:161], v[20:23], v[222:225], v[158:161]
	v_mfma_f32_16x16x32_f16 v[210:213], v[20:23], v[226:229], v[210:213]
	v_mfma_f32_16x16x32_f16 v[166:169], v[20:23], v[230:233], v[166:169]
	v_mfma_f32_16x16x32_f16 v[190:193], v[24:27], v[218:221], v[190:193]
	v_mfma_f32_16x16x32_f16 v[202:205], v[24:27], v[222:225], v[202:205]
	v_mfma_f32_16x16x32_f16 v[206:209], v[24:27], v[226:229], v[206:209]
	v_mfma_f32_16x16x32_f16 v[214:217], v[24:27], v[230:233], v[214:217]
	s_setprio 0
	ds_read_b128 v[218:221], v128 offset:32768
	ds_read_b128 v[222:225], v128 offset:34816
	ds_read_b128 v[226:229], v128 offset:36864
	ds_read_b128 v[230:233], v128 offset:38912
	ds_read_b128 v[24:27], v130 offset:32768
	ds_read_b128 v[246:249], v130 offset:34816
	v_cvt_pk_f16_f32 v21, v80, v81
	v_cvt_pk_f16_f32 v20, v78, v79
	ds_write_b64 v100, v[20:21] offset:16384
	s_add_u32 s0, s22, 0x80600
	s_addc_u32 s1, s90, 0
	global_load_dwordx4 v[20:23], v201, s[0:1] nt
	s_setprio 1
	s_waitcnt lgkmcnt(1)
	v_mfma_f32_16x16x32_f16 v[78:81], v[24:27], v[218:221], v[242:245]
	v_mfma_f32_16x16x32_f16 v[104:107], v[24:27], v[226:229], v[104:107]
	v_mfma_f32_16x16x32_f16 v[108:111], v[246:249], v[218:221], v[108:111]
	v_mfma_f32_16x16x32_f16 v[112:115], v[246:249], v[222:225], v[112:115]
	v_mfma_f32_16x16x32_f16 v[116:119], v[246:249], v[226:229], v[116:119]
	v_mfma_f32_16x16x32_f16 v[242:245], v[24:27], v[222:225], v[30:33]
	v_mfma_f32_16x16x32_f16 v[234:237], v[24:27], v[230:233], v[234:237]
	v_mfma_f32_16x16x32_f16 v[238:241], v[246:249], v[230:233], v[238:241]
	s_setprio 0
	ds_read_b128 v[28:31], v130 offset:36864
	ds_read_b128 v[32:35], v130 offset:38912
	v_cvt_pk_f16_f32 v25, v84, v85
	v_cvt_pk_f16_f32 v24, v82, v83
	ds_write_b64 v100, v[24:25] offset:20480
	s_add_u32 s0, s22, 0xa0600
	s_addc_u32 s1, s90, 0
	global_load_dwordx4 v[24:27], v201, s[0:1] nt
	s_setprio 1
	s_waitcnt lgkmcnt(1)
	v_mfma_f32_16x16x32_f16 v[82:85], v[28:31], v[218:221], v[40:43]
	v_mfma_f32_16x16x32_f16 v[120:123], v[28:31], v[230:233], v[120:123]
	v_mfma_f32_16x16x32_f16 v[124:127], v[32:35], v[218:221], v[124:127]
	v_mfma_f32_16x16x32_f16 v[146:149], v[32:35], v[222:225], v[146:149]
	v_mfma_f32_16x16x32_f16 v[134:137], v[32:35], v[230:233], v[134:137]
	v_mfma_f32_16x16x32_f16 v[138:141], v[28:31], v[222:225], v[138:141]
	v_mfma_f32_16x16x32_f16 v[142:145], v[28:31], v[226:229], v[142:145]
	v_mfma_f32_16x16x32_f16 v[150:153], v[32:35], v[226:229], v[150:153]
	s_setprio 0
	ds_read_b128 v[32:35], v130 offset:40960
	ds_read_b128 v[40:43], v130 offset:43008
	v_cvt_pk_f16_f32 v29, v88, v89
	v_cvt_pk_f16_f32 v28, v86, v87
	ds_write_b64 v100, v[28:29] offset:24576
	s_add_u32 s0, s22, 0xc0600
	s_addc_u32 s1, s90, 0
	global_load_dwordx4 v[28:31], v201, s[0:1] nt
	s_setprio 1
	s_waitcnt lgkmcnt(1)
	v_mfma_f32_16x16x32_f16 v[86:89], v[32:35], v[218:221], v[44:47]
	v_mfma_f32_16x16x32_f16 v[170:173], v[32:35], v[222:225], v[170:173]
	v_mfma_f32_16x16x32_f16 v[174:177], v[32:35], v[226:229], v[174:177]
	v_mfma_f32_16x16x32_f16 v[162:165], v[32:35], v[230:233], v[162:165]
	v_mfma_f32_16x16x32_f16 v[178:181], v[40:43], v[218:221], v[178:181]
	v_mfma_f32_16x16x32_f16 v[182:185], v[40:43], v[222:225], v[182:185]
	v_mfma_f32_16x16x32_f16 v[186:189], v[40:43], v[226:229], v[186:189]
	v_mfma_f32_16x16x32_f16 v[154:157], v[40:43], v[230:233], v[154:157]
	s_setprio 0
	ds_read_b128 v[40:43], v130 offset:45056
	ds_read_b128 v[44:47], v130 offset:47104
	v_cvt_pk_f16_f32 v33, v92, v93
	v_cvt_pk_f16_f32 v32, v90, v91
	ds_write_b64 v100, v[32:33] offset:28672
	s_add_u32 s0, s22, 0xe0600
	s_addc_u32 s1, s90, 0
	global_load_dwordx4 v[32:35], v201, s[0:1] nt
	s_setprio 1
	s_waitcnt lgkmcnt(1)
	v_mfma_f32_16x16x32_f16 v[74:77], v[40:43], v[218:221], v[74:77]
	v_mfma_f32_16x16x32_f16 v[90:93], v[40:43], v[222:225], v[158:161]
	v_mfma_f32_16x16x32_f16 v[158:161], v[40:43], v[226:229], v[210:213]
	v_mfma_f32_16x16x32_f16 v[166:169], v[40:43], v[230:233], v[166:169]
	v_mfma_f32_16x16x32_f16 v[190:193], v[44:47], v[218:221], v[190:193]
	v_mfma_f32_16x16x32_f16 v[202:205], v[44:47], v[222:225], v[202:205]
	v_mfma_f32_16x16x32_f16 v[206:209], v[44:47], v[226:229], v[206:209]
	v_mfma_f32_16x16x32_f16 v[210:213], v[44:47], v[230:233], v[214:217]
	s_setprio 0
	s_waitcnt vmcnt(4)
	s_waitcnt lgkmcnt(0)
	s_barrier
	s_nop 0
	ds_read_b128 v[214:217], v131
	ds_read_b128 v[218:221], v131 offset:2048
	ds_read_b128 v[222:225], v131 offset:4096
	ds_read_b128 v[226:229], v131 offset:6144
	ds_read_b128 v[40:43], v129
	ds_read_b128 v[44:47], v129 offset:2048
	s_add_u32 s70, s22, 0x700
	s_addc_u32 s71, s90, 0
	v_lshl_add_u64 v[198:199], s[36:37], 0, v[196:197]
	v_readfirstlane_b32 s0, v95
	s_mov_b32 m0, s0
	v_cvt_pk_f16_f32 v7, v6, v7
	global_load_lds_dwordx4 v[198:199], off
	v_cvt_pk_f16_f32 v6, v4, v5
	ds_write_b64 v100, v[6:7] offset:32768
	global_load_dwordx4 v[4:7], v201, s[70:71] nt
	s_setprio 1
	s_waitcnt lgkmcnt(1)
	v_mfma_f32_16x16x32_f16 v[78:81], v[40:43], v[214:217], v[78:81]
	v_mfma_f32_16x16x32_f16 v[104:107], v[40:43], v[222:225], v[104:107]
	v_mfma_f32_16x16x32_f16 v[108:111], v[44:47], v[214:217], v[108:111]
	v_mfma_f32_16x16x32_f16 v[112:115], v[44:47], v[218:221], v[112:115]
	v_mfma_f32_16x16x32_f16 v[116:119], v[44:47], v[222:225], v[116:119]
	v_mfma_f32_16x16x32_f16 v[230:233], v[40:43], v[218:221], v[242:245]
	v_mfma_f32_16x16x32_f16 v[234:237], v[40:43], v[226:229], v[234:237]
	v_mfma_f32_16x16x32_f16 v[238:241], v[44:47], v[226:229], v[238:241]
	s_setprio 0
	ds_read_b128 v[44:47], v129 offset:4096
	ds_read_b128 v[242:245], v129 offset:6144
	v_readfirstlane_b32 s72, v96
	v_lshl_add_u64 v[40:41], v[198:199], 0, s[58:59]
	s_mov_b32 m0, s72
	s_nop 0
	global_load_lds_dwordx4 v[40:41], off
	v_cvt_pk_f16_f32 v41, v52, v53
	v_cvt_pk_f16_f32 v40, v50, v51
	ds_write_b64 v100, v[40:41] offset:36864
	s_add_u32 s70, s22, 0x20700
	s_addc_u32 s71, s90, 0
	global_load_dwordx4 v[40:43], v201, s[70:71] nt
	s_setprio 1
	s_waitcnt lgkmcnt(1)
	v_mfma_f32_16x16x32_f16 v[82:85], v[44:47], v[214:217], v[82:85]
	v_mfma_f32_16x16x32_f16 v[120:123], v[44:47], v[226:229], v[120:123]
	v_mfma_f32_16x16x32_f16 v[124:127], v[242:245], v[214:217], v[124:127]
	v_mfma_f32_16x16x32_f16 v[146:149], v[242:245], v[218:221], v[146:149]
	v_mfma_f32_16x16x32_f16 v[134:137], v[242:245], v[226:229], v[134:137]
	v_mfma_f32_16x16x32_f16 v[138:141], v[44:47], v[218:221], v[138:141]
	v_mfma_f32_16x16x32_f16 v[142:145], v[44:47], v[222:225], v[142:145]
	v_mfma_f32_16x16x32_f16 v[150:153], v[242:245], v[222:225], v[150:153]
	s_setprio 0
	ds_read_b128 v[48:51], v129 offset:8192
	ds_read_b128 v[242:245], v129 offset:10240
	v_readfirstlane_b32 s71, v97
	v_lshl_add_u64 v[44:45], v[198:199], 0, s[60:61]
	s_mov_b32 m0, s71
	s_nop 0
	global_load_lds_dwordx4 v[44:45], off
	v_cvt_pk_f16_f32 v45, v56, v57
	v_cvt_pk_f16_f32 v44, v54, v55
	ds_write_b64 v100, v[44:45] offset:40960
	s_add_u32 s80, s22, 0x40700
	s_addc_u32 s81, s90, 0
	global_load_dwordx4 v[44:47], v201, s[80:81] nt
	s_setprio 1
	s_waitcnt lgkmcnt(1)
	v_mfma_f32_16x16x32_f16 v[86:89], v[48:51], v[214:217], v[86:89]
	v_mfma_f32_16x16x32_f16 v[170:173], v[48:51], v[218:221], v[170:173]
	v_mfma_f32_16x16x32_f16 v[174:177], v[48:51], v[222:225], v[174:177]
	v_mfma_f32_16x16x32_f16 v[162:165], v[48:51], v[226:229], v[162:165]
	v_mfma_f32_16x16x32_f16 v[178:181], v[242:245], v[214:217], v[178:181]
	v_mfma_f32_16x16x32_f16 v[182:185], v[242:245], v[218:221], v[182:185]
	v_mfma_f32_16x16x32_f16 v[186:189], v[242:245], v[222:225], v[186:189]
	v_mfma_f32_16x16x32_f16 v[154:157], v[242:245], v[226:229], v[154:157]
	s_setprio 0
	ds_read_b128 v[52:55], v129 offset:12288
	ds_read_b128 v[242:245], v129 offset:14336
	v_readfirstlane_b32 s70, v98
	v_lshl_add_u64 v[48:49], v[198:199], 0, s[62:63]
	s_mov_b32 m0, s70
	s_nop 0
	global_load_lds_dwordx4 v[48:49], off
	v_cvt_pk_f16_f32 v49, v60, v61
	v_cvt_pk_f16_f32 v48, v58, v59
	ds_write_b64 v100, v[48:49] offset:45056
	s_add_u32 s80, s22, 0x60700
	s_addc_u32 s81, s90, 0
	global_load_dwordx4 v[48:51], v201, s[80:81] nt
	s_setprio 1
	s_waitcnt lgkmcnt(1)
	v_mfma_f32_16x16x32_f16 v[74:77], v[52:55], v[214:217], v[74:77]
	v_mfma_f32_16x16x32_f16 v[90:93], v[52:55], v[218:221], v[90:93]
	v_mfma_f32_16x16x32_f16 v[158:161], v[52:55], v[222:225], v[158:161]
	v_mfma_f32_16x16x32_f16 v[166:169], v[52:55], v[226:229], v[166:169]
	v_mfma_f32_16x16x32_f16 v[190:193], v[242:245], v[214:217], v[190:193]
	v_mfma_f32_16x16x32_f16 v[202:205], v[242:245], v[218:221], v[202:205]
	v_mfma_f32_16x16x32_f16 v[206:209], v[242:245], v[222:225], v[206:209]
	v_mfma_f32_16x16x32_f16 v[210:213], v[242:245], v[226:229], v[210:213]
	s_setprio 0
	ds_read_b128 v[214:217], v128
	ds_read_b128 v[218:221], v128 offset:2048
	ds_read_b128 v[222:225], v128 offset:4096
	ds_read_b128 v[226:229], v128 offset:6144
	ds_read_b128 v[56:59], v130
	ds_read_b128 v[242:245], v130 offset:2048
	v_cvt_pk_f16_f32 v53, v64, v65
	v_cvt_pk_f16_f32 v52, v62, v63
	ds_write_b64 v100, v[52:53] offset:49152
	s_add_u32 s80, s22, 0x80700
	s_addc_u32 s81, s90, 0
	global_load_dwordx4 v[52:55], v201, s[80:81] nt
	s_setprio 1
	s_waitcnt lgkmcnt(1)
	v_mfma_f32_16x16x32_f16 v[78:81], v[56:59], v[214:217], v[78:81]
	v_mfma_f32_16x16x32_f16 v[104:107], v[56:59], v[222:225], v[104:107]
	v_mfma_f32_16x16x32_f16 v[108:111], v[242:245], v[214:217], v[108:111]
	v_mfma_f32_16x16x32_f16 v[112:115], v[242:245], v[218:221], v[112:115]
	v_mfma_f32_16x16x32_f16 v[116:119], v[242:245], v[222:225], v[116:119]
	v_mfma_f32_16x16x32_f16 v[230:233], v[56:59], v[218:221], v[230:233]
	v_mfma_f32_16x16x32_f16 v[234:237], v[56:59], v[226:229], v[234:237]
	v_mfma_f32_16x16x32_f16 v[238:241], v[242:245], v[226:229], v[238:241]
	s_setprio 0
	ds_read_b128 v[60:63], v130 offset:4096
	ds_read_b128 v[242:245], v130 offset:6144
	v_cvt_pk_f16_f32 v57, v68, v69
	v_cvt_pk_f16_f32 v56, v66, v67
	ds_write_b64 v100, v[56:57] offset:53248
	s_add_u32 s80, s22, 0xa0700
	s_addc_u32 s81, s90, 0
	global_load_dwordx4 v[56:59], v201, s[80:81] nt
	s_setprio 1
	s_waitcnt lgkmcnt(1)
	v_mfma_f32_16x16x32_f16 v[82:85], v[60:63], v[214:217], v[82:85]
	v_mfma_f32_16x16x32_f16 v[120:123], v[60:63], v[226:229], v[120:123]
	v_mfma_f32_16x16x32_f16 v[124:127], v[242:245], v[214:217], v[124:127]
	v_mfma_f32_16x16x32_f16 v[146:149], v[242:245], v[218:221], v[146:149]
	v_mfma_f32_16x16x32_f16 v[134:137], v[242:245], v[226:229], v[134:137]
	v_mfma_f32_16x16x32_f16 v[138:141], v[60:63], v[218:221], v[138:141]
	v_mfma_f32_16x16x32_f16 v[142:145], v[60:63], v[222:225], v[142:145]
	v_mfma_f32_16x16x32_f16 v[150:153], v[242:245], v[222:225], v[150:153]
	s_setprio 0
	ds_read_b128 v[64:67], v130 offset:8192
	ds_read_b128 v[242:245], v130 offset:10240
	v_cvt_pk_f16_f32 v61, v72, v73
	v_cvt_pk_f16_f32 v60, v70, v71
	ds_write_b64 v100, v[60:61] offset:57344
	s_add_u32 s80, s22, 0xc0700
	s_addc_u32 s81, s90, 0
	global_load_dwordx4 v[60:63], v201, s[80:81] nt
	s_setprio 1
	s_waitcnt lgkmcnt(1)
	v_mfma_f32_16x16x32_f16 v[86:89], v[64:67], v[214:217], v[86:89]
	v_mfma_f32_16x16x32_f16 v[170:173], v[64:67], v[218:221], v[170:173]
	v_mfma_f32_16x16x32_f16 v[174:177], v[64:67], v[222:225], v[174:177]
	v_mfma_f32_16x16x32_f16 v[162:165], v[64:67], v[226:229], v[162:165]
	v_mfma_f32_16x16x32_f16 v[178:181], v[242:245], v[214:217], v[178:181]
	v_mfma_f32_16x16x32_f16 v[182:185], v[242:245], v[218:221], v[182:185]
	v_mfma_f32_16x16x32_f16 v[186:189], v[242:245], v[222:225], v[186:189]
	v_mfma_f32_16x16x32_f16 v[154:157], v[242:245], v[226:229], v[154:157]
	s_setprio 0
	ds_read_b128 v[64:67], v130 offset:12288
	ds_read_b128 v[68:71], v130 offset:14336
	v_cvt_pk_f16_f32 v39, v38, v39
	v_cvt_pk_f16_f32 v38, v36, v37
	ds_write_b64 v100, v[38:39] offset:61440
	s_add_u32 s80, s22, 0xe0700
	s_addc_u32 s81, s90, 0
	global_load_dwordx4 v[36:39], v201, s[80:81] nt
	s_setprio 1
	s_waitcnt lgkmcnt(1)
	v_mfma_f32_16x16x32_f16 v[90:93], v[64:67], v[218:221], v[90:93]
	v_mfma_f32_16x16x32_f16 v[242:245], v[64:67], v[214:217], v[74:77]
	v_mfma_f32_16x16x32_f16 v[158:161], v[64:67], v[222:225], v[158:161]
	v_mfma_f32_16x16x32_f16 v[166:169], v[64:67], v[226:229], v[166:169]
	v_mfma_f32_16x16x32_f16 v[190:193], v[68:71], v[214:217], v[190:193]
	v_mfma_f32_16x16x32_f16 v[202:205], v[68:71], v[218:221], v[202:205]
	v_mfma_f32_16x16x32_f16 v[206:209], v[68:71], v[222:225], v[206:209]
	v_mfma_f32_16x16x32_f16 v[210:213], v[68:71], v[226:229], v[210:213]
	s_setprio 0
	s_waitcnt vmcnt(4)
	s_waitcnt lgkmcnt(0)
	s_barrier
	ds_read_b128 v[214:217], v131 offset:32768
	ds_read_b128 v[218:221], v131 offset:34816
	ds_read_b128 v[222:225], v131 offset:36864
	ds_read_b128 v[226:229], v131 offset:38912
	ds_read_b128 v[64:67], v129 offset:32768
	ds_read_b128 v[68:71], v129 offset:34816
	s_add_u32 s80, s22, 0x800
	s_addc_u32 s81, s90, 0
	v_lshl_add_u64 v[198:199], s[38:39], 0, v[196:197]
	v_readfirstlane_b32 s1, v94
	s_mov_b32 m0, s1
	v_cvt_pk_f16_f32 v3, v2, v3
	global_load_lds_dwordx4 v[198:199], off
	v_cvt_pk_f16_f32 v2, v0, v1
	ds_write_b64 v100, v[2:3]
	global_load_dwordx4 v[0:3], v201, s[80:81] nt
	s_setprio 1
	s_waitcnt lgkmcnt(1)
	v_mfma_f32_16x16x32_f16 v[104:107], v[64:67], v[222:225], v[104:107]
	v_mfma_f32_16x16x32_f16 v[108:111], v[68:71], v[214:217], v[108:111]
	v_mfma_f32_16x16x32_f16 v[112:115], v[68:71], v[218:221], v[112:115]
	v_mfma_f32_16x16x32_f16 v[116:119], v[68:71], v[222:225], v[116:119]
	v_mfma_f32_16x16x32_f16 v[246:249], v[64:67], v[214:217], v[78:81]
	v_mfma_f32_16x16x32_f16 v[230:233], v[64:67], v[218:221], v[230:233]
	v_mfma_f32_16x16x32_f16 v[234:237], v[64:67], v[226:229], v[234:237]
	v_mfma_f32_16x16x32_f16 v[238:241], v[68:71], v[226:229], v[238:241]
	s_setprio 0
	ds_read_b128 v[68:71], v129 offset:36864
	ds_read_b128 v[72:75], v129 offset:38912
	v_readfirstlane_b32 s92, v99
	v_lshl_add_u64 v[64:65], v[198:199], 0, s[58:59]
	s_mov_b32 m0, s92
	v_cvt_pk_f16_f32 v11, v10, v11
	global_load_lds_dwordx4 v[64:65], off
	v_cvt_pk_f16_f32 v10, v8, v9
	ds_write_b64 v100, v[10:11] offset:4096
	s_add_u32 s80, s22, 0x20800
	s_addc_u32 s81, s90, 0
	global_load_dwordx4 v[64:67], v201, s[80:81] nt
	s_setprio 1
	s_waitcnt lgkmcnt(1)
	v_mfma_f32_16x16x32_f16 v[8:11], v[68:71], v[214:217], v[82:85]
	v_mfma_f32_16x16x32_f16 v[120:123], v[68:71], v[226:229], v[120:123]
	v_mfma_f32_16x16x32_f16 v[124:127], v[72:75], v[214:217], v[124:127]
	v_mfma_f32_16x16x32_f16 v[146:149], v[72:75], v[218:221], v[146:149]
	v_mfma_f32_16x16x32_f16 v[134:137], v[72:75], v[226:229], v[134:137]
	v_mfma_f32_16x16x32_f16 v[138:141], v[68:71], v[218:221], v[138:141]
	v_mfma_f32_16x16x32_f16 v[142:145], v[68:71], v[222:225], v[142:145]
	v_mfma_f32_16x16x32_f16 v[150:153], v[72:75], v[222:225], v[150:153]
	s_setprio 0
	ds_read_b128 v[72:75], v129 offset:40960
	ds_read_b128 v[76:79], v129 offset:43008
	v_readfirstlane_b32 s91, v101
	v_lshl_add_u64 v[68:69], v[198:199], 0, s[60:61]
	s_mov_b32 m0, s91
	v_cvt_pk_f16_f32 v15, v14, v15
	global_load_lds_dwordx4 v[68:69], off
	v_cvt_pk_f16_f32 v14, v12, v13
	ds_write_b64 v100, v[14:15] offset:8192
	s_add_u32 s80, s22, 0x40800
	s_addc_u32 s81, s90, 0
	global_load_dwordx4 v[68:71], v201, s[80:81] nt
	s_setprio 1
	s_waitcnt lgkmcnt(1)
	v_mfma_f32_16x16x32_f16 v[12:15], v[72:75], v[214:217], v[86:89]
	v_mfma_f32_16x16x32_f16 v[170:173], v[72:75], v[218:221], v[170:173]
	v_mfma_f32_16x16x32_f16 v[174:177], v[72:75], v[222:225], v[174:177]
	v_mfma_f32_16x16x32_f16 v[162:165], v[72:75], v[226:229], v[162:165]
	v_mfma_f32_16x16x32_f16 v[178:181], v[76:79], v[214:217], v[178:181]
	v_mfma_f32_16x16x32_f16 v[182:185], v[76:79], v[218:221], v[182:185]
	v_mfma_f32_16x16x32_f16 v[186:189], v[76:79], v[222:225], v[186:189]
	v_mfma_f32_16x16x32_f16 v[154:157], v[76:79], v[226:229], v[154:157]
	s_setprio 0
	ds_read_b128 v[76:79], v129 offset:45056
	ds_read_b128 v[80:83], v129 offset:47104
	v_readfirstlane_b32 s73, v102
	v_lshl_add_u64 v[72:73], v[198:199], 0, s[62:63]
	s_mov_b32 m0, s73
	v_cvt_pk_f16_f32 v19, v18, v19
	global_load_lds_dwordx4 v[72:73], off
	v_cvt_pk_f16_f32 v18, v16, v17
	ds_write_b64 v100, v[18:19] offset:12288
	s_add_u32 s80, s22, 0x60800
	s_addc_u32 s81, s90, 0
	global_load_dwordx4 v[72:75], v201, s[80:81] nt
	s_setprio 1
	s_waitcnt lgkmcnt(1)
	v_mfma_f32_16x16x32_f16 v[16:19], v[76:79], v[214:217], v[242:245]
	v_mfma_f32_16x16x32_f16 v[242:245], v[76:79], v[218:221], v[90:93]
	v_mfma_f32_16x16x32_f16 v[158:161], v[76:79], v[222:225], v[158:161]
	v_mfma_f32_16x16x32_f16 v[166:169], v[76:79], v[226:229], v[166:169]
	v_mfma_f32_16x16x32_f16 v[190:193], v[80:83], v[214:217], v[190:193]
	v_mfma_f32_16x16x32_f16 v[202:205], v[80:83], v[218:221], v[202:205]
	v_mfma_f32_16x16x32_f16 v[206:209], v[80:83], v[222:225], v[206:209]
	v_mfma_f32_16x16x32_f16 v[210:213], v[80:83], v[226:229], v[210:213]
	s_setprio 0
	ds_read_b128 v[214:217], v128 offset:32768
	ds_read_b128 v[218:221], v128 offset:34816
	ds_read_b128 v[222:225], v128 offset:36864
	ds_read_b128 v[226:229], v128 offset:38912
	ds_read_b128 v[80:83], v130 offset:32768
	ds_read_b128 v[84:87], v130 offset:34816
	v_cvt_pk_f16_f32 v23, v22, v23
	v_cvt_pk_f16_f32 v22, v20, v21
	ds_write_b64 v100, v[22:23] offset:16384
	s_add_u32 s80, s22, 0x80800
	s_addc_u32 s81, s90, 0
	global_load_dwordx4 v[76:79], v201, s[80:81] nt
	s_setprio 1
	s_waitcnt lgkmcnt(1)
	v_mfma_f32_16x16x32_f16 v[20:23], v[80:83], v[214:217], v[246:249]
	v_mfma_f32_16x16x32_f16 v[104:107], v[80:83], v[222:225], v[104:107]
	v_mfma_f32_16x16x32_f16 v[108:111], v[84:87], v[214:217], v[108:111]
	v_mfma_f32_16x16x32_f16 v[112:115], v[84:87], v[218:221], v[112:115]
	v_mfma_f32_16x16x32_f16 v[116:119], v[84:87], v[222:225], v[116:119]
	v_mfma_f32_16x16x32_f16 v[230:233], v[80:83], v[218:221], v[230:233]
	v_mfma_f32_16x16x32_f16 v[234:237], v[80:83], v[226:229], v[234:237]
	v_mfma_f32_16x16x32_f16 v[238:241], v[84:87], v[226:229], v[238:241]
	s_setprio 0
	ds_read_b128 v[84:87], v130 offset:36864
	ds_read_b128 v[88:91], v130 offset:38912
	v_cvt_pk_f16_f32 v27, v26, v27
	v_cvt_pk_f16_f32 v26, v24, v25
	ds_write_b64 v100, v[26:27] offset:20480
	s_add_u32 s80, s22, 0xa0800
	s_addc_u32 s81, s90, 0
	global_load_dwordx4 v[80:83], v201, s[80:81] nt
	s_setprio 1
	s_waitcnt lgkmcnt(1)
	v_mfma_f32_16x16x32_f16 v[24:27], v[84:87], v[214:217], v[8:11]
	v_mfma_f32_16x16x32_f16 v[120:123], v[84:87], v[226:229], v[120:123]
	v_mfma_f32_16x16x32_f16 v[124:127], v[88:91], v[214:217], v[124:127]
	v_mfma_f32_16x16x32_f16 v[146:149], v[88:91], v[218:221], v[146:149]
	v_mfma_f32_16x16x32_f16 v[134:137], v[88:91], v[226:229], v[134:137]
	v_mfma_f32_16x16x32_f16 v[138:141], v[84:87], v[218:221], v[138:141]
	v_mfma_f32_16x16x32_f16 v[142:145], v[84:87], v[222:225], v[142:145]
	v_mfma_f32_16x16x32_f16 v[150:153], v[88:91], v[222:225], v[150:153]
	s_setprio 0
	ds_read_b128 v[8:11], v130 offset:40960
	ds_read_b128 v[88:91], v130 offset:43008
	v_cvt_pk_f16_f32 v31, v30, v31
	v_cvt_pk_f16_f32 v30, v28, v29
	ds_write_b64 v100, v[30:31] offset:24576
	s_add_u32 s80, s22, 0xc0800
	s_addc_u32 s81, s90, 0
	global_load_dwordx4 v[84:87], v201, s[80:81] nt
	s_setprio 1
	s_waitcnt lgkmcnt(1)
	v_mfma_f32_16x16x32_f16 v[12:15], v[8:11], v[214:217], v[12:15]
	v_mfma_f32_16x16x32_f16 v[28:31], v[8:11], v[218:221], v[170:173]
	v_mfma_f32_16x16x32_f16 v[170:173], v[8:11], v[222:225], v[174:177]
	v_mfma_f32_16x16x32_f16 v[162:165], v[8:11], v[226:229], v[162:165]
	v_mfma_f32_16x16x32_f16 v[174:177], v[88:91], v[214:217], v[178:181]
	v_mfma_f32_16x16x32_f16 v[178:181], v[88:91], v[218:221], v[182:185]
	v_mfma_f32_16x16x32_f16 v[182:185], v[88:91], v[222:225], v[186:189]
	v_mfma_f32_16x16x32_f16 v[154:157], v[88:91], v[226:229], v[154:157]
	s_setprio 0
	ds_read_b128 v[8:11], v130 offset:45056
	ds_read_b128 v[186:189], v130 offset:47104
	v_cvt_pk_f16_f32 v35, v34, v35
	v_cvt_pk_f16_f32 v34, v32, v33
	ds_write_b64 v100, v[34:35] offset:28672
	s_add_u32 s80, s22, 0xe0800
	s_addc_u32 s81, s90, 0
	global_load_dwordx4 v[88:91], v201, s[80:81] nt
	s_setprio 1
	s_waitcnt lgkmcnt(1)
	v_mfma_f32_16x16x32_f16 v[16:19], v[8:11], v[214:217], v[16:19]
	v_mfma_f32_16x16x32_f16 v[32:35], v[8:11], v[218:221], v[242:245]
	v_mfma_f32_16x16x32_f16 v[158:161], v[8:11], v[222:225], v[158:161]
	v_mfma_f32_16x16x32_f16 v[166:169], v[8:11], v[226:229], v[166:169]
	v_mfma_f32_16x16x32_f16 v[190:193], v[186:189], v[214:217], v[190:193]
	v_mfma_f32_16x16x32_f16 v[202:205], v[186:189], v[218:221], v[202:205]
	v_mfma_f32_16x16x32_f16 v[206:209], v[186:189], v[222:225], v[206:209]
	v_mfma_f32_16x16x32_f16 v[186:189], v[186:189], v[226:229], v[210:213]
	s_setprio 0
	s_waitcnt vmcnt(4)
	s_waitcnt lgkmcnt(0)
	s_barrier
	s_nop 0
	ds_read_b128 v[210:213], v131
	ds_read_b128 v[214:217], v131 offset:2048
	ds_read_b128 v[218:221], v131 offset:4096
	ds_read_b128 v[222:225], v131 offset:6144
	ds_read_b128 v[8:11], v129
	ds_read_b128 v[226:229], v129 offset:2048
	s_add_u32 s80, s22, 0x900
	v_lshl_add_u64 v[92:93], s[40:41], 0, v[196:197]
	s_addc_u32 s81, s90, 0
	s_mov_b32 m0, s0
	v_cvt_pk_f16_f32 v7, v6, v7
	global_load_lds_dwordx4 v[92:93], off
	v_cvt_pk_f16_f32 v6, v4, v5
	ds_write_b64 v100, v[6:7] offset:32768
	global_load_dwordx4 v[4:7], v201, s[80:81] nt
	s_setprio 1
	s_waitcnt lgkmcnt(1)
	v_mfma_f32_16x16x32_f16 v[20:23], v[8:11], v[210:213], v[20:23]
	v_mfma_f32_16x16x32_f16 v[104:107], v[8:11], v[218:221], v[104:107]
	v_mfma_f32_16x16x32_f16 v[108:111], v[226:229], v[210:213], v[108:111]
	v_mfma_f32_16x16x32_f16 v[112:115], v[226:229], v[214:217], v[112:115]
	v_mfma_f32_16x16x32_f16 v[116:119], v[226:229], v[218:221], v[116:119]
	v_mfma_f32_16x16x32_f16 v[230:233], v[8:11], v[214:217], v[230:233]
	v_mfma_f32_16x16x32_f16 v[234:237], v[8:11], v[222:225], v[234:237]
	v_mfma_f32_16x16x32_f16 v[226:229], v[226:229], v[222:225], v[238:241]
	s_setprio 0
	s_nop 1
	ds_read_b128 v[238:241], v129 offset:4096
	ds_read_b128 v[242:245], v129 offset:6144
	s_mov_b32 m0, s72
	v_lshl_add_u64 v[8:9], v[92:93], 0, s[58:59]
	global_load_lds_dwordx4 v[8:9], off
	v_cvt_pk_f16_f32 v9, v42, v43
	v_cvt_pk_f16_f32 v8, v40, v41
	ds_write_b64 v100, v[8:9] offset:36864
	s_add_u32 s80, s22, 0x20900
	s_addc_u32 s81, s90, 0
	global_load_dwordx4 v[8:11], v201, s[80:81] nt
	s_setprio 1
	s_waitcnt lgkmcnt(1)
	v_mfma_f32_16x16x32_f16 v[24:27], v[238:241], v[210:213], v[24:27]
	v_mfma_f32_16x16x32_f16 v[120:123], v[238:241], v[222:225], v[120:123]
	v_mfma_f32_16x16x32_f16 v[124:127], v[242:245], v[210:213], v[124:127]
	v_mfma_f32_16x16x32_f16 v[146:149], v[242:245], v[214:217], v[146:149]
	v_mfma_f32_16x16x32_f16 v[134:137], v[242:245], v[222:225], v[134:137]
	v_mfma_f32_16x16x32_f16 v[138:141], v[238:241], v[214:217], v[138:141]
	v_mfma_f32_16x16x32_f16 v[142:145], v[238:241], v[218:221], v[142:145]
	v_mfma_f32_16x16x32_f16 v[150:153], v[242:245], v[218:221], v[150:153]
	s_setprio 0
	ds_read_b128 v[238:241], v129 offset:8192
	ds_read_b128 v[242:245], v129 offset:10240
	s_mov_b32 m0, s71
	v_lshl_add_u64 v[40:41], v[92:93], 0, s[60:61]
	global_load_lds_dwordx4 v[40:41], off
	v_cvt_pk_f16_f32 v41, v46, v47
	v_cvt_pk_f16_f32 v40, v44, v45
	ds_write_b64 v100, v[40:41] offset:40960
	s_add_u32 s80, s22, 0x40900
	s_addc_u32 s81, s90, 0
	global_load_dwordx4 v[40:43], v201, s[80:81] nt
	s_setprio 1
	s_waitcnt lgkmcnt(1)
	v_mfma_f32_16x16x32_f16 v[12:15], v[238:241], v[210:213], v[12:15]
	v_mfma_f32_16x16x32_f16 v[28:31], v[238:241], v[214:217], v[28:31]
	v_mfma_f32_16x16x32_f16 v[170:173], v[238:241], v[218:221], v[170:173]
	v_mfma_f32_16x16x32_f16 v[162:165], v[238:241], v[222:225], v[162:165]
	v_mfma_f32_16x16x32_f16 v[174:177], v[242:245], v[210:213], v[174:177]
	v_mfma_f32_16x16x32_f16 v[178:181], v[242:245], v[214:217], v[178:181]
	v_mfma_f32_16x16x32_f16 v[182:185], v[242:245], v[218:221], v[182:185]
	v_mfma_f32_16x16x32_f16 v[154:157], v[242:245], v[222:225], v[154:157]
	s_setprio 0
	ds_read_b128 v[238:241], v129 offset:12288
	ds_read_b128 v[242:245], v129 offset:14336
	s_mov_b32 m0, s70
	v_lshl_add_u64 v[44:45], v[92:93], 0, s[62:63]
	global_load_lds_dwordx4 v[44:45], off
	v_cvt_pk_f16_f32 v45, v50, v51
	v_cvt_pk_f16_f32 v44, v48, v49
	ds_write_b64 v100, v[44:45] offset:45056
	s_add_u32 s70, s22, 0x60900
	s_addc_u32 s71, s90, 0
	global_load_dwordx4 v[44:47], v201, s[70:71] nt
	s_setprio 1
	s_waitcnt lgkmcnt(1)
	v_mfma_f32_16x16x32_f16 v[16:19], v[238:241], v[210:213], v[16:19]
	v_mfma_f32_16x16x32_f16 v[32:35], v[238:241], v[214:217], v[32:35]
	v_mfma_f32_16x16x32_f16 v[158:161], v[238:241], v[218:221], v[158:161]
	v_mfma_f32_16x16x32_f16 v[166:169], v[238:241], v[222:225], v[166:169]
	v_mfma_f32_16x16x32_f16 v[190:193], v[242:245], v[210:213], v[190:193]
	v_mfma_f32_16x16x32_f16 v[202:205], v[242:245], v[214:217], v[202:205]
	v_mfma_f32_16x16x32_f16 v[206:209], v[242:245], v[218:221], v[206:209]
	v_mfma_f32_16x16x32_f16 v[186:189], v[242:245], v[222:225], v[186:189]
	s_setprio 0
	ds_read_b128 v[210:213], v128
	ds_read_b128 v[214:217], v128 offset:2048
	ds_read_b128 v[218:221], v128 offset:4096
	ds_read_b128 v[222:225], v128 offset:6144
	ds_read_b128 v[238:241], v130
	ds_read_b128 v[242:245], v130 offset:2048
	v_cvt_pk_f16_f32 v49, v54, v55
	v_cvt_pk_f16_f32 v48, v52, v53
	ds_write_b64 v100, v[48:49] offset:49152
	s_add_u32 s70, s22, 0x80900
	s_addc_u32 s71, s90, 0
	global_load_dwordx4 v[48:51], v201, s[70:71] nt
	s_setprio 1
	s_waitcnt lgkmcnt(1)
	v_mfma_f32_16x16x32_f16 v[20:23], v[238:241], v[210:213], v[20:23]
	v_mfma_f32_16x16x32_f16 v[104:107], v[238:241], v[218:221], v[104:107]
	v_mfma_f32_16x16x32_f16 v[108:111], v[242:245], v[210:213], v[108:111]
	v_mfma_f32_16x16x32_f16 v[112:115], v[242:245], v[214:217], v[112:115]
	v_mfma_f32_16x16x32_f16 v[116:119], v[242:245], v[218:221], v[116:119]
	v_mfma_f32_16x16x32_f16 v[230:233], v[238:241], v[214:217], v[230:233]
	v_mfma_f32_16x16x32_f16 v[234:237], v[238:241], v[222:225], v[234:237]
	v_mfma_f32_16x16x32_f16 v[226:229], v[242:245], v[222:225], v[226:229]
	s_setprio 0
	ds_read_b128 v[238:241], v130 offset:4096
	ds_read_b128 v[242:245], v130 offset:6144
	v_cvt_pk_f16_f32 v53, v58, v59
	v_cvt_pk_f16_f32 v52, v56, v57
	ds_write_b64 v100, v[52:53] offset:53248
	s_add_u32 s70, s22, 0xa0900
	s_addc_u32 s71, s90, 0
	global_load_dwordx4 v[52:55], v201, s[70:71] nt
	s_setprio 1
	s_waitcnt lgkmcnt(1)
	v_mfma_f32_16x16x32_f16 v[24:27], v[238:241], v[210:213], v[24:27]
	v_mfma_f32_16x16x32_f16 v[120:123], v[238:241], v[222:225], v[120:123]
	v_mfma_f32_16x16x32_f16 v[124:127], v[242:245], v[210:213], v[124:127]
	v_mfma_f32_16x16x32_f16 v[146:149], v[242:245], v[214:217], v[146:149]
	v_mfma_f32_16x16x32_f16 v[134:137], v[242:245], v[222:225], v[134:137]
	v_mfma_f32_16x16x32_f16 v[138:141], v[238:241], v[214:217], v[138:141]
	v_mfma_f32_16x16x32_f16 v[142:145], v[238:241], v[218:221], v[142:145]
	v_mfma_f32_16x16x32_f16 v[150:153], v[242:245], v[218:221], v[150:153]
	s_setprio 0
	ds_read_b128 v[238:241], v130 offset:8192
	ds_read_b128 v[242:245], v130 offset:10240
	v_cvt_pk_f16_f32 v57, v62, v63
	v_cvt_pk_f16_f32 v56, v60, v61
	ds_write_b64 v100, v[56:57] offset:57344
	s_add_u32 s70, s22, 0xc0900
	s_addc_u32 s71, s90, 0
	global_load_dwordx4 v[56:59], v201, s[70:71] nt
	s_setprio 1
	s_waitcnt lgkmcnt(1)
	v_mfma_f32_16x16x32_f16 v[28:31], v[238:241], v[214:217], v[28:31]
	v_mfma_f32_16x16x32_f16 v[246:249], v[238:241], v[210:213], v[12:15]
	v_mfma_f32_16x16x32_f16 v[170:173], v[238:241], v[218:221], v[170:173]
	v_mfma_f32_16x16x32_f16 v[162:165], v[238:241], v[222:225], v[162:165]
	v_mfma_f32_16x16x32_f16 v[174:177], v[242:245], v[210:213], v[174:177]
	v_mfma_f32_16x16x32_f16 v[178:181], v[242:245], v[214:217], v[178:181]
	v_mfma_f32_16x16x32_f16 v[182:185], v[242:245], v[218:221], v[182:185]
	v_mfma_f32_16x16x32_f16 v[154:157], v[242:245], v[222:225], v[154:157]
	s_setprio 0
	ds_read_b128 v[12:15], v130 offset:12288
	ds_read_b128 v[238:241], v130 offset:14336
	v_cvt_pk_f16_f32 v39, v38, v39
	v_cvt_pk_f16_f32 v38, v36, v37
	ds_write_b64 v100, v[38:39] offset:61440
	s_add_u32 s70, s22, 0xe0900
	s_addc_u32 s71, s90, 0
	global_load_dwordx4 v[60:63], v201, s[70:71] nt
	s_setprio 1
	s_waitcnt lgkmcnt(1)
	v_mfma_f32_16x16x32_f16 v[36:39], v[12:15], v[210:213], v[16:19]
	v_mfma_f32_16x16x32_f16 v[32:35], v[12:15], v[214:217], v[32:35]
	v_mfma_f32_16x16x32_f16 v[158:161], v[12:15], v[218:221], v[158:161]
	v_mfma_f32_16x16x32_f16 v[166:169], v[12:15], v[222:225], v[166:169]
	v_mfma_f32_16x16x32_f16 v[190:193], v[238:241], v[210:213], v[190:193]
	v_mfma_f32_16x16x32_f16 v[202:205], v[238:241], v[214:217], v[202:205]
	v_mfma_f32_16x16x32_f16 v[206:209], v[238:241], v[218:221], v[206:209]
	v_mfma_f32_16x16x32_f16 v[186:189], v[238:241], v[222:225], v[186:189]
	s_setprio 0
	s_waitcnt vmcnt(4)
	s_waitcnt lgkmcnt(0)
	s_barrier
	ds_read_b128 v[210:213], v131 offset:32768
	ds_read_b128 v[214:217], v131 offset:34816
	ds_read_b128 v[218:221], v131 offset:36864
	ds_read_b128 v[222:225], v131 offset:38912
	ds_read_b128 v[12:15], v129 offset:32768
	ds_read_b128 v[16:19], v129 offset:34816
	s_add_u32 s70, s22, 0xa00
	v_lshl_add_u64 v[92:93], s[42:43], 0, v[196:197]
	s_addc_u32 s71, s90, 0
	s_mov_b32 m0, s1
	v_cvt_pk_f16_f32 v3, v2, v3
	global_load_lds_dwordx4 v[92:93], off
	v_cvt_pk_f16_f32 v2, v0, v1
	ds_write_b64 v100, v[2:3]
	global_load_dwordx4 v[0:3], v201, s[70:71] nt
	s_setprio 1
	s_waitcnt lgkmcnt(1)
	v_mfma_f32_16x16x32_f16 v[104:107], v[12:15], v[218:221], v[104:107]
	v_mfma_f32_16x16x32_f16 v[108:111], v[16:19], v[210:213], v[108:111]
	v_mfma_f32_16x16x32_f16 v[112:115], v[16:19], v[214:217], v[112:115]
	v_mfma_f32_16x16x32_f16 v[116:119], v[16:19], v[218:221], v[116:119]
	v_mfma_f32_16x16x32_f16 v[238:241], v[12:15], v[210:213], v[20:23]
	v_mfma_f32_16x16x32_f16 v[230:233], v[12:15], v[214:217], v[230:233]
	v_mfma_f32_16x16x32_f16 v[234:237], v[12:15], v[222:225], v[234:237]
	v_mfma_f32_16x16x32_f16 v[226:229], v[16:19], v[222:225], v[226:229]
	s_setprio 0
	ds_read_b128 v[16:19], v129 offset:36864
	ds_read_b128 v[20:23], v129 offset:38912
	s_mov_b32 m0, s92
	v_lshl_add_u64 v[12:13], v[92:93], 0, s[58:59]
	global_load_lds_dwordx4 v[12:13], off
	v_cvt_pk_f16_f32 v13, v66, v67
	v_cvt_pk_f16_f32 v12, v64, v65
	ds_write_b64 v100, v[12:13] offset:4096
	s_add_u32 s0, s22, 0x20a00
	s_addc_u32 s1, s90, 0
	global_load_dwordx4 v[12:15], v201, s[0:1] nt
	s_setprio 1
	s_waitcnt lgkmcnt(1)
	v_mfma_f32_16x16x32_f16 v[64:67], v[16:19], v[210:213], v[24:27]
	v_mfma_f32_16x16x32_f16 v[120:123], v[16:19], v[222:225], v[120:123]
	v_mfma_f32_16x16x32_f16 v[124:127], v[20:23], v[210:213], v[124:127]
	v_mfma_f32_16x16x32_f16 v[146:149], v[20:23], v[214:217], v[146:149]
	v_mfma_f32_16x16x32_f16 v[134:137], v[20:23], v[222:225], v[134:137]
	v_mfma_f32_16x16x32_f16 v[138:141], v[16:19], v[214:217], v[138:141]
	v_mfma_f32_16x16x32_f16 v[142:145], v[16:19], v[218:221], v[142:145]
	v_mfma_f32_16x16x32_f16 v[150:153], v[20:23], v[218:221], v[150:153]
	s_setprio 0
	ds_read_b128 v[20:23], v129 offset:40960
	ds_read_b128 v[24:27], v129 offset:43008
	s_mov_b32 m0, s91
	v_lshl_add_u64 v[16:17], v[92:93], 0, s[60:61]
	global_load_lds_dwordx4 v[16:17], off
	v_cvt_pk_f16_f32 v17, v70, v71
	v_cvt_pk_f16_f32 v16, v68, v69
	ds_write_b64 v100, v[16:17] offset:8192
	s_add_u32 s0, s22, 0x40a00
	s_addc_u32 s1, s90, 0
	global_load_dwordx4 v[16:19], v201, s[0:1] nt
	s_setprio 1
	s_waitcnt lgkmcnt(1)
	v_mfma_f32_16x16x32_f16 v[68:71], v[20:23], v[210:213], v[246:249]
	v_mfma_f32_16x16x32_f16 v[242:245], v[20:23], v[214:217], v[28:31]
	v_mfma_f32_16x16x32_f16 v[170:173], v[20:23], v[218:221], v[170:173]
	v_mfma_f32_16x16x32_f16 v[162:165], v[20:23], v[222:225], v[162:165]
	v_mfma_f32_16x16x32_f16 v[174:177], v[24:27], v[210:213], v[174:177]
	v_mfma_f32_16x16x32_f16 v[178:181], v[24:27], v[214:217], v[178:181]
	v_mfma_f32_16x16x32_f16 v[182:185], v[24:27], v[218:221], v[182:185]
	v_mfma_f32_16x16x32_f16 v[154:157], v[24:27], v[222:225], v[154:157]
	s_setprio 0
	ds_read_b128 v[24:27], v129 offset:45056
	ds_read_b128 v[28:31], v129 offset:47104
	s_mov_b32 m0, s73
	v_lshl_add_u64 v[20:21], v[92:93], 0, s[62:63]
	global_load_lds_dwordx4 v[20:21], off
	v_cvt_pk_f16_f32 v21, v74, v75
	v_cvt_pk_f16_f32 v20, v72, v73
	ds_write_b64 v100, v[20:21] offset:12288
	s_add_u32 s0, s22, 0x60a00
	s_addc_u32 s1, s90, 0
	global_load_dwordx4 v[20:23], v201, s[0:1] nt
	s_setprio 1
	s_waitcnt lgkmcnt(1)
	v_mfma_f32_16x16x32_f16 v[72:75], v[24:27], v[210:213], v[36:39]
	v_mfma_f32_16x16x32_f16 v[246:249], v[24:27], v[214:217], v[32:35]
	v_mfma_f32_16x16x32_f16 v[158:161], v[24:27], v[218:221], v[158:161]
	v_mfma_f32_16x16x32_f16 v[166:169], v[24:27], v[222:225], v[166:169]
	v_mfma_f32_16x16x32_f16 v[190:193], v[28:31], v[210:213], v[190:193]
	v_mfma_f32_16x16x32_f16 v[202:205], v[28:31], v[214:217], v[202:205]
	v_mfma_f32_16x16x32_f16 v[206:209], v[28:31], v[218:221], v[206:209]
	v_mfma_f32_16x16x32_f16 v[186:189], v[28:31], v[222:225], v[186:189]
	s_setprio 0
	ds_read_b128 v[210:213], v128 offset:32768
	ds_read_b128 v[214:217], v128 offset:34816
	ds_read_b128 v[218:221], v128 offset:36864
	ds_read_b128 v[222:225], v128 offset:38912
	ds_read_b128 v[28:31], v130 offset:32768
	ds_read_b128 v[32:35], v130 offset:34816
	v_cvt_pk_f16_f32 v25, v78, v79
	v_cvt_pk_f16_f32 v24, v76, v77
	ds_write_b64 v100, v[24:25] offset:16384
	s_add_u32 s0, s22, 0x80a00
	s_addc_u32 s1, s90, 0
	global_load_dwordx4 v[24:27], v201, s[0:1] nt
	s_setprio 1
	s_waitcnt lgkmcnt(1)
	v_mfma_f32_16x16x32_f16 v[76:79], v[28:31], v[210:213], v[238:241]
	v_mfma_f32_16x16x32_f16 v[104:107], v[28:31], v[218:221], v[104:107]
	v_mfma_f32_16x16x32_f16 v[108:111], v[32:35], v[210:213], v[108:111]
	v_mfma_f32_16x16x32_f16 v[112:115], v[32:35], v[214:217], v[112:115]
	v_mfma_f32_16x16x32_f16 v[116:119], v[32:35], v[218:221], v[116:119]
	v_mfma_f32_16x16x32_f16 v[230:233], v[28:31], v[214:217], v[230:233]
	v_mfma_f32_16x16x32_f16 v[234:237], v[28:31], v[222:225], v[234:237]
	v_mfma_f32_16x16x32_f16 v[226:229], v[32:35], v[222:225], v[226:229]
	s_setprio 0
	ds_read_b128 v[32:35], v130 offset:36864
	ds_read_b128 v[36:39], v130 offset:38912
	v_cvt_pk_f16_f32 v29, v82, v83
	v_cvt_pk_f16_f32 v28, v80, v81
	ds_write_b64 v100, v[28:29] offset:20480
	s_add_u32 s0, s22, 0xa0a00
	s_addc_u32 s1, s90, 0
	global_load_dwordx4 v[28:31], v201, s[0:1] nt
	s_setprio 1
	s_waitcnt lgkmcnt(1)
	v_mfma_f32_16x16x32_f16 v[80:83], v[32:35], v[210:213], v[64:67]
	v_mfma_f32_16x16x32_f16 v[120:123], v[32:35], v[222:225], v[120:123]
	v_mfma_f32_16x16x32_f16 v[124:127], v[36:39], v[210:213], v[124:127]
	v_mfma_f32_16x16x32_f16 v[146:149], v[36:39], v[214:217], v[146:149]
	v_mfma_f32_16x16x32_f16 v[134:137], v[36:39], v[222:225], v[134:137]
	v_mfma_f32_16x16x32_f16 v[138:141], v[32:35], v[214:217], v[138:141]
	v_mfma_f32_16x16x32_f16 v[142:145], v[32:35], v[218:221], v[142:145]
	v_mfma_f32_16x16x32_f16 v[150:153], v[36:39], v[218:221], v[150:153]
	s_setprio 0
	ds_read_b128 v[36:39], v130 offset:40960
	ds_read_b128 v[64:67], v130 offset:43008
	v_cvt_pk_f16_f32 v33, v86, v87
	v_cvt_pk_f16_f32 v32, v84, v85
	ds_write_b64 v100, v[32:33] offset:24576
	s_add_u32 s0, s22, 0xc0a00
	s_addc_u32 s1, s90, 0
	global_load_dwordx4 v[32:35], v201, s[0:1] nt
	s_setprio 1
	s_waitcnt lgkmcnt(1)
	v_mfma_f32_16x16x32_f16 v[68:71], v[36:39], v[210:213], v[68:71]
	v_mfma_f32_16x16x32_f16 v[84:87], v[36:39], v[214:217], v[242:245]
	v_mfma_f32_16x16x32_f16 v[170:173], v[36:39], v[218:221], v[170:173]
	v_mfma_f32_16x16x32_f16 v[162:165], v[36:39], v[222:225], v[162:165]
	v_mfma_f32_16x16x32_f16 v[174:177], v[64:67], v[210:213], v[174:177]
	v_mfma_f32_16x16x32_f16 v[178:181], v[64:67], v[214:217], v[178:181]
	v_mfma_f32_16x16x32_f16 v[182:185], v[64:67], v[218:221], v[182:185]
	v_mfma_f32_16x16x32_f16 v[154:157], v[64:67], v[222:225], v[154:157]
	s_setprio 0
	ds_read_b128 v[64:67], v130 offset:45056
	ds_read_b128 v[238:241], v130 offset:47104
	v_cvt_pk_f16_f32 v37, v90, v91
	v_cvt_pk_f16_f32 v36, v88, v89
	ds_write_b64 v100, v[36:37] offset:28672
	s_add_u32 s0, s22, 0xe0a00
	s_addc_u32 s1, s90, 0
	global_load_dwordx4 v[36:39], v201, s[0:1] nt
	s_setprio 1
	s_waitcnt lgkmcnt(1)
	v_mfma_f32_16x16x32_f16 v[72:75], v[64:67], v[210:213], v[72:75]
	v_mfma_f32_16x16x32_f16 v[88:91], v[64:67], v[214:217], v[246:249]
	v_mfma_f32_16x16x32_f16 v[158:161], v[64:67], v[218:221], v[158:161]
	v_mfma_f32_16x16x32_f16 v[166:169], v[64:67], v[222:225], v[166:169]
	v_mfma_f32_16x16x32_f16 v[190:193], v[238:241], v[210:213], v[190:193]
	v_mfma_f32_16x16x32_f16 v[202:205], v[238:241], v[214:217], v[202:205]
	v_mfma_f32_16x16x32_f16 v[206:209], v[238:241], v[218:221], v[206:209]
	v_mfma_f32_16x16x32_f16 v[186:189], v[238:241], v[222:225], v[186:189]
	s_setprio 0
	s_waitcnt vmcnt(4)
	s_waitcnt lgkmcnt(0)
	s_barrier
	ds_read_b128 v[210:213], v131
	ds_read_b128 v[214:217], v131 offset:2048
	ds_read_b128 v[218:221], v131 offset:4096
	ds_read_b128 v[222:225], v131 offset:6144
	ds_read_b128 v[64:67], v129
	ds_read_b128 v[238:241], v129 offset:2048
	s_add_u32 s70, s22, 0xb00
	v_lshl_add_u64 v[92:93], s[44:45], 0, v[196:197]
	s_addc_u32 s71, s90, 0
	v_readfirstlane_b32 s0, v95
	s_mov_b32 m0, s0
	v_cvt_pk_f16_f32 v7, v6, v7
	global_load_lds_dwordx4 v[92:93], off
	v_cvt_pk_f16_f32 v6, v4, v5
	ds_write_b64 v100, v[6:7] offset:32768
	global_load_dwordx4 v[4:7], v201, s[70:71] nt
	s_setprio 1
	s_waitcnt lgkmcnt(1)
	v_mfma_f32_16x16x32_f16 v[76:79], v[64:67], v[210:213], v[76:79]
	v_mfma_f32_16x16x32_f16 v[104:107], v[64:67], v[218:221], v[104:107]
	v_mfma_f32_16x16x32_f16 v[108:111], v[238:241], v[210:213], v[108:111]
	v_mfma_f32_16x16x32_f16 v[112:115], v[238:241], v[214:217], v[112:115]
	v_mfma_f32_16x16x32_f16 v[116:119], v[238:241], v[218:221], v[116:119]
	v_mfma_f32_16x16x32_f16 v[230:233], v[64:67], v[214:217], v[230:233]
	v_mfma_f32_16x16x32_f16 v[234:237], v[64:67], v[222:225], v[234:237]
	v_mfma_f32_16x16x32_f16 v[226:229], v[238:241], v[222:225], v[226:229]
	s_setprio 0
	ds_read_b128 v[238:241], v129 offset:4096
	ds_read_b128 v[242:245], v129 offset:6144
	v_readfirstlane_b32 s72, v96
	v_lshl_add_u64 v[64:65], v[92:93], 0, s[58:59]
	s_mov_b32 m0, s72
	v_cvt_pk_f16_f32 v11, v10, v11
	global_load_lds_dwordx4 v[64:65], off
	v_cvt_pk_f16_f32 v10, v8, v9
	ds_write_b64 v100, v[10:11] offset:36864
	s_add_u32 s70, s22, 0x20b00
	s_addc_u32 s71, s90, 0
	global_load_dwordx4 v[64:67], v201, s[70:71] nt
	s_setprio 1
	s_waitcnt lgkmcnt(1)
	v_mfma_f32_16x16x32_f16 v[8:11], v[238:241], v[210:213], v[80:83]
	v_mfma_f32_16x16x32_f16 v[80:83], v[238:241], v[214:217], v[138:141]
	v_mfma_f32_16x16x32_f16 v[138:141], v[238:241], v[218:221], v[142:145]
	v_mfma_f32_16x16x32_f16 v[120:123], v[238:241], v[222:225], v[120:123]
	v_mfma_f32_16x16x32_f16 v[124:127], v[242:245], v[210:213], v[124:127]
	v_mfma_f32_16x16x32_f16 v[142:145], v[242:245], v[214:217], v[146:149]
	v_mfma_f32_16x16x32_f16 v[146:149], v[242:245], v[218:221], v[150:153]
	v_mfma_f32_16x16x32_f16 v[134:137], v[242:245], v[222:225], v[134:137]
	s_setprio 0
	s_nop 0
	ds_read_b128 v[150:153], v129 offset:8192
	ds_read_b128 v[238:241], v129 offset:10240
	v_readfirstlane_b32 s71, v97
	v_lshl_add_u64 v[198:199], v[92:93], 0, s[60:61]
	s_mov_b32 m0, s71
	v_cvt_pk_f16_f32 v43, v42, v43
	global_load_lds_dwordx4 v[198:199], off
	v_cvt_pk_f16_f32 v42, v40, v41
	ds_write_b64 v100, v[42:43] offset:40960
	s_add_u32 s80, s22, 0x40b00
	s_addc_u32 s81, s90, 0
	global_load_dwordx4 v[40:43], v201, s[80:81] nt
	s_setprio 1
	s_waitcnt lgkmcnt(1)
	v_mfma_f32_16x16x32_f16 v[68:71], v[150:153], v[210:213], v[68:71]
	v_mfma_f32_16x16x32_f16 v[84:87], v[150:153], v[214:217], v[84:87]
	v_mfma_f32_16x16x32_f16 v[170:173], v[150:153], v[218:221], v[170:173]
	v_mfma_f32_16x16x32_f16 v[150:153], v[150:153], v[222:225], v[162:165]
	v_mfma_f32_16x16x32_f16 v[162:165], v[238:241], v[210:213], v[174:177]
	v_mfma_f32_16x16x32_f16 v[174:177], v[238:241], v[214:217], v[178:181]
	v_mfma_f32_16x16x32_f16 v[178:181], v[238:241], v[218:221], v[182:185]
	v_mfma_f32_16x16x32_f16 v[154:157], v[238:241], v[222:225], v[154:157]
	s_setprio 0
	s_nop 0
	ds_read_b128 v[182:185], v129 offset:12288
	ds_read_b128 v[238:241], v129 offset:14336
	v_readfirstlane_b32 s70, v98
	v_lshl_add_u64 v[92:93], v[92:93], 0, s[62:63]
	s_mov_b32 m0, s70
	v_cvt_pk_f16_f32 v47, v46, v47
	global_load_lds_dwordx4 v[92:93], off
	v_cvt_pk_f16_f32 v46, v44, v45
	ds_write_b64 v100, v[46:47] offset:45056
	s_add_u32 s80, s22, 0x60b00
	s_addc_u32 s81, s90, 0
	global_load_dwordx4 v[44:47], v201, s[80:81] nt
	s_setprio 1
	s_waitcnt lgkmcnt(1)
	v_mfma_f32_16x16x32_f16 v[72:75], v[182:185], v[210:213], v[72:75]
	v_mfma_f32_16x16x32_f16 v[88:91], v[182:185], v[214:217], v[88:91]
	v_mfma_f32_16x16x32_f16 v[158:161], v[182:185], v[218:221], v[158:161]
	v_mfma_f32_16x16x32_f16 v[166:169], v[182:185], v[222:225], v[166:169]
	v_mfma_f32_16x16x32_f16 v[182:185], v[238:241], v[210:213], v[190:193]
	v_mfma_f32_16x16x32_f16 v[190:193], v[238:241], v[214:217], v[202:205]
	v_mfma_f32_16x16x32_f16 v[202:205], v[238:241], v[218:221], v[206:209]
	v_mfma_f32_16x16x32_f16 v[186:189], v[238:241], v[222:225], v[186:189]
	s_setprio 0
	s_nop 0
	ds_read_b128 v[206:209], v128
	ds_read_b128 v[210:213], v128 offset:2048
	ds_read_b128 v[214:217], v128 offset:4096
	ds_read_b128 v[218:221], v128 offset:6144
	ds_read_b128 v[222:225], v130
	ds_read_b128 v[238:241], v130 offset:2048
	v_cvt_pk_f16_f32 v51, v50, v51
	v_cvt_pk_f16_f32 v50, v48, v49
	ds_write_b64 v100, v[50:51] offset:49152
	s_add_u32 s80, s22, 0x80b00
	s_addc_u32 s81, s90, 0
	global_load_dwordx4 v[48:51], v201, s[80:81] nt
	s_setprio 1
	s_waitcnt lgkmcnt(1)
	v_mfma_f32_16x16x32_f16 v[76:79], v[222:225], v[206:209], v[76:79]
	v_mfma_f32_16x16x32_f16 v[104:107], v[222:225], v[214:217], v[104:107]
	v_mfma_f32_16x16x32_f16 v[108:111], v[238:241], v[206:209], v[108:111]
	v_mfma_f32_16x16x32_f16 v[112:115], v[238:241], v[210:213], v[112:115]
	v_mfma_f32_16x16x32_f16 v[116:119], v[238:241], v[214:217], v[116:119]
	v_mfma_f32_16x16x32_f16 v[230:233], v[222:225], v[210:213], v[230:233]
	v_mfma_f32_16x16x32_f16 v[222:225], v[222:225], v[218:221], v[234:237]
	v_mfma_f32_16x16x32_f16 v[226:229], v[238:241], v[218:221], v[226:229]
	s_setprio 0
	s_nop 0
	ds_read_b128 v[234:237], v130 offset:4096
	ds_read_b128 v[238:241], v130 offset:6144
	v_cvt_pk_f16_f32 v55, v54, v55
	v_cvt_pk_f16_f32 v54, v52, v53
	ds_write_b64 v100, v[54:55] offset:53248
	s_add_u32 s80, s22, 0xa0b00
	s_addc_u32 s81, s90, 0
	global_load_dwordx4 v[52:55], v201, s[80:81] nt
	s_setprio 1
	s_waitcnt lgkmcnt(1)
	v_mfma_f32_16x16x32_f16 v[80:83], v[234:237], v[210:213], v[80:83]
	v_mfma_f32_16x16x32_f16 v[120:123], v[234:237], v[218:221], v[120:123]
	v_mfma_f32_16x16x32_f16 v[124:127], v[238:241], v[206:209], v[124:127]
	v_mfma_f32_16x16x32_f16 v[146:149], v[238:241], v[214:217], v[146:149]
	v_mfma_f32_16x16x32_f16 v[134:137], v[238:241], v[218:221], v[134:137]
	v_mfma_f32_16x16x32_f16 v[242:245], v[234:237], v[206:209], v[8:11]
	v_mfma_f32_16x16x32_f16 v[138:141], v[234:237], v[214:217], v[138:141]
	v_mfma_f32_16x16x32_f16 v[142:145], v[238:241], v[210:213], v[142:145]
	s_setprio 0
	ds_read_b128 v[8:11], v130 offset:8192
	ds_read_b128 v[234:237], v130 offset:10240
	v_cvt_pk_f16_f32 v59, v58, v59
	v_cvt_pk_f16_f32 v58, v56, v57
	ds_write_b64 v100, v[58:59] offset:57344
	s_add_u32 s80, s22, 0xc0b00
	s_addc_u32 s81, s90, 0
	global_load_dwordx4 v[56:59], v201, s[80:81] nt
	s_setprio 1
	s_waitcnt lgkmcnt(1)
	v_mfma_f32_16x16x32_f16 v[84:87], v[8:11], v[210:213], v[84:87]
	v_mfma_f32_16x16x32_f16 v[238:241], v[8:11], v[206:209], v[68:71]
	v_mfma_f32_16x16x32_f16 v[170:173], v[8:11], v[214:217], v[170:173]
	v_mfma_f32_16x16x32_f16 v[150:153], v[8:11], v[218:221], v[150:153]
	v_mfma_f32_16x16x32_f16 v[162:165], v[234:237], v[206:209], v[162:165]
	v_mfma_f32_16x16x32_f16 v[174:177], v[234:237], v[210:213], v[174:177]
	v_mfma_f32_16x16x32_f16 v[178:181], v[234:237], v[214:217], v[178:181]
	v_mfma_f32_16x16x32_f16 v[154:157], v[234:237], v[218:221], v[154:157]
	s_setprio 0
	ds_read_b128 v[8:11], v130 offset:12288
	ds_read_b128 v[68:71], v130 offset:14336
	v_cvt_pk_f16_f32 v63, v62, v63
	v_cvt_pk_f16_f32 v62, v60, v61
	ds_write_b64 v100, v[62:63] offset:61440
	s_add_u32 s80, s22, 0xe0b00
	s_addc_u32 s81, s90, 0
	global_load_dwordx4 v[60:63], v201, s[80:81] nt
	s_setprio 1
	s_waitcnt lgkmcnt(1)
	v_mfma_f32_16x16x32_f16 v[88:91], v[8:11], v[210:213], v[88:91]
	v_mfma_f32_16x16x32_f16 v[234:237], v[8:11], v[206:209], v[72:75]
	v_mfma_f32_16x16x32_f16 v[158:161], v[8:11], v[214:217], v[158:161]
	v_mfma_f32_16x16x32_f16 v[166:169], v[8:11], v[218:221], v[166:169]
	v_mfma_f32_16x16x32_f16 v[182:185], v[68:71], v[206:209], v[182:185]
	v_mfma_f32_16x16x32_f16 v[190:193], v[68:71], v[210:213], v[190:193]
	v_mfma_f32_16x16x32_f16 v[202:205], v[68:71], v[214:217], v[202:205]
	v_mfma_f32_16x16x32_f16 v[186:189], v[68:71], v[218:221], v[186:189]
	s_setprio 0
	s_waitcnt vmcnt(4)
	s_waitcnt lgkmcnt(0)
	s_barrier
	ds_read_b128 v[206:209], v131 offset:32768
	ds_read_b128 v[210:213], v131 offset:34816
	ds_read_b128 v[214:217], v131 offset:36864
	ds_read_b128 v[218:221], v131 offset:38912
	ds_read_b128 v[68:71], v129 offset:32768
	ds_read_b128 v[72:75], v129 offset:34816
	s_add_u32 s80, s22, 0xc00
	v_lshl_add_u64 v[92:93], s[46:47], 0, v[196:197]
	s_addc_u32 s81, s90, 0
	v_readfirstlane_b32 s1, v94
	s_mov_b32 m0, s1
	v_cvt_pk_f16_f32 v3, v2, v3
	global_load_lds_dwordx4 v[92:93], off
	v_cvt_pk_f16_f32 v2, v0, v1
	ds_write_b64 v100, v[2:3]
	global_load_dwordx4 v[8:11], v201, s[80:81] nt
	s_setprio 1
	s_waitcnt lgkmcnt(1)
	v_mfma_f32_16x16x32_f16 v[0:3], v[68:71], v[206:209], v[76:79]
	v_mfma_f32_16x16x32_f16 v[104:107], v[68:71], v[214:217], v[104:107]
	v_mfma_f32_16x16x32_f16 v[108:111], v[72:75], v[206:209], v[108:111]
	v_mfma_f32_16x16x32_f16 v[112:115], v[72:75], v[210:213], v[112:115]
	v_mfma_f32_16x16x32_f16 v[116:119], v[72:75], v[214:217], v[116:119]
	v_mfma_f32_16x16x32_f16 v[230:233], v[68:71], v[210:213], v[230:233]
	v_mfma_f32_16x16x32_f16 v[222:225], v[68:71], v[218:221], v[222:225]
	v_mfma_f32_16x16x32_f16 v[226:229], v[72:75], v[218:221], v[226:229]
	s_setprio 0
	ds_read_b128 v[72:75], v129 offset:36864
	ds_read_b128 v[76:79], v129 offset:38912
	v_readfirstlane_b32 s92, v99
	v_lshl_add_u64 v[68:69], v[92:93], 0, s[58:59]
	s_mov_b32 m0, s92
	v_cvt_pk_f16_f32 v15, v14, v15
	global_load_lds_dwordx4 v[68:69], off
	v_cvt_pk_f16_f32 v14, v12, v13
	ds_write_b64 v100, v[14:15] offset:4096
	s_add_u32 s80, s22, 0x20c00
	s_addc_u32 s81, s90, 0
	global_load_dwordx4 v[68:71], v201, s[80:81] nt
	s_setprio 1
	s_waitcnt lgkmcnt(1)
	v_mfma_f32_16x16x32_f16 v[12:15], v[72:75], v[206:209], v[242:245]
	v_mfma_f32_16x16x32_f16 v[120:123], v[72:75], v[218:221], v[120:123]
	v_mfma_f32_16x16x32_f16 v[124:127], v[76:79], v[206:209], v[124:127]
	v_mfma_f32_16x16x32_f16 v[146:149], v[76:79], v[214:217], v[146:149]
	v_mfma_f32_16x16x32_f16 v[134:137], v[76:79], v[218:221], v[134:137]
	v_mfma_f32_16x16x32_f16 v[242:245], v[72:75], v[210:213], v[80:83]
	v_mfma_f32_16x16x32_f16 v[138:141], v[72:75], v[214:217], v[138:141]
	v_mfma_f32_16x16x32_f16 v[142:145], v[76:79], v[210:213], v[142:145]
	s_setprio 0
	ds_read_b128 v[76:79], v129 offset:40960
	ds_read_b128 v[80:83], v129 offset:43008
	v_readfirstlane_b32 s91, v101
	v_lshl_add_u64 v[72:73], v[92:93], 0, s[60:61]
	s_mov_b32 m0, s91
	v_cvt_pk_f16_f32 v19, v18, v19
	global_load_lds_dwordx4 v[72:73], off
	v_cvt_pk_f16_f32 v18, v16, v17
	ds_write_b64 v100, v[18:19] offset:8192
	s_add_u32 s80, s22, 0x40c00
	s_addc_u32 s81, s90, 0
	global_load_dwordx4 v[72:75], v201, s[80:81] nt
	s_setprio 1
	s_waitcnt lgkmcnt(1)
	v_mfma_f32_16x16x32_f16 v[16:19], v[76:79], v[206:209], v[238:241]
	v_mfma_f32_16x16x32_f16 v[238:241], v[76:79], v[210:213], v[84:87]
	v_mfma_f32_16x16x32_f16 v[170:173], v[76:79], v[214:217], v[170:173]
	v_mfma_f32_16x16x32_f16 v[150:153], v[76:79], v[218:221], v[150:153]
	v_mfma_f32_16x16x32_f16 v[162:165], v[80:83], v[206:209], v[162:165]
	v_mfma_f32_16x16x32_f16 v[174:177], v[80:83], v[210:213], v[174:177]
	v_mfma_f32_16x16x32_f16 v[178:181], v[80:83], v[214:217], v[178:181]
	v_mfma_f32_16x16x32_f16 v[154:157], v[80:83], v[218:221], v[154:157]
	s_setprio 0
	ds_read_b128 v[80:83], v129 offset:45056
	ds_read_b128 v[84:87], v129 offset:47104
	v_readfirstlane_b32 s73, v102
	v_lshl_add_u64 v[76:77], v[92:93], 0, s[62:63]
	s_mov_b32 m0, s73
	v_cvt_pk_f16_f32 v23, v22, v23
	global_load_lds_dwordx4 v[76:77], off
	v_cvt_pk_f16_f32 v22, v20, v21
	ds_write_b64 v100, v[22:23] offset:12288
	s_add_u32 s80, s22, 0x60c00
	s_addc_u32 s81, s90, 0
	global_load_dwordx4 v[76:79], v201, s[80:81] nt
	s_setprio 1
	s_waitcnt lgkmcnt(1)
	v_mfma_f32_16x16x32_f16 v[20:23], v[80:83], v[206:209], v[234:237]
	v_mfma_f32_16x16x32_f16 v[234:237], v[80:83], v[210:213], v[88:91]
	v_mfma_f32_16x16x32_f16 v[158:161], v[80:83], v[214:217], v[158:161]
	v_mfma_f32_16x16x32_f16 v[166:169], v[80:83], v[218:221], v[166:169]
	v_mfma_f32_16x16x32_f16 v[182:185], v[84:87], v[206:209], v[182:185]
	v_mfma_f32_16x16x32_f16 v[190:193], v[84:87], v[210:213], v[190:193]
	v_mfma_f32_16x16x32_f16 v[202:205], v[84:87], v[214:217], v[202:205]
	v_mfma_f32_16x16x32_f16 v[186:189], v[84:87], v[218:221], v[186:189]
	s_setprio 0
	ds_read_b128 v[206:209], v128 offset:32768
	ds_read_b128 v[210:213], v128 offset:34816
	ds_read_b128 v[214:217], v128 offset:36864
	ds_read_b128 v[218:221], v128 offset:38912
	ds_read_b128 v[84:87], v130 offset:32768
	ds_read_b128 v[88:91], v130 offset:34816
	v_cvt_pk_f16_f32 v27, v26, v27
	v_cvt_pk_f16_f32 v26, v24, v25
	ds_write_b64 v100, v[26:27] offset:16384
	s_add_u32 s80, s22, 0x80c00
	s_addc_u32 s81, s90, 0
	global_load_dwordx4 v[80:83], v201, s[80:81] nt
	s_setprio 1
	s_waitcnt lgkmcnt(1)
	v_mfma_f32_16x16x32_f16 v[24:27], v[84:87], v[206:209], v[0:3]
	v_mfma_f32_16x16x32_f16 v[104:107], v[84:87], v[214:217], v[104:107]
	v_mfma_f32_16x16x32_f16 v[108:111], v[88:91], v[206:209], v[108:111]
	v_mfma_f32_16x16x32_f16 v[112:115], v[88:91], v[210:213], v[112:115]
	v_mfma_f32_16x16x32_f16 v[116:119], v[88:91], v[214:217], v[116:119]
	v_mfma_f32_16x16x32_f16 v[230:233], v[84:87], v[210:213], v[230:233]
	v_mfma_f32_16x16x32_f16 v[222:225], v[84:87], v[218:221], v[222:225]
	v_mfma_f32_16x16x32_f16 v[226:229], v[88:91], v[218:221], v[226:229]
	s_setprio 0
	ds_read_b128 v[0:3], v130 offset:36864
	ds_read_b128 v[88:91], v130 offset:38912
	v_cvt_pk_f16_f32 v31, v30, v31
	v_cvt_pk_f16_f32 v30, v28, v29
	ds_write_b64 v100, v[30:31] offset:20480
	s_add_u32 s80, s22, 0xa0c00
	s_addc_u32 s81, s90, 0
	global_load_dwordx4 v[84:87], v201, s[80:81] nt
	s_setprio 1
	s_waitcnt lgkmcnt(1)
	v_mfma_f32_16x16x32_f16 v[12:15], v[0:3], v[206:209], v[12:15]
	v_mfma_f32_16x16x32_f16 v[28:31], v[0:3], v[210:213], v[242:245]
	v_mfma_f32_16x16x32_f16 v[120:123], v[0:3], v[218:221], v[120:123]
	v_mfma_f32_16x16x32_f16 v[124:127], v[88:91], v[206:209], v[124:127]
	v_mfma_f32_16x16x32_f16 v[146:149], v[88:91], v[214:217], v[146:149]
	v_mfma_f32_16x16x32_f16 v[134:137], v[88:91], v[218:221], v[134:137]
	v_mfma_f32_16x16x32_f16 v[138:141], v[0:3], v[214:217], v[138:141]
	v_mfma_f32_16x16x32_f16 v[142:145], v[88:91], v[210:213], v[142:145]
	s_setprio 0
	ds_read_b128 v[0:3], v130 offset:40960
	ds_read_b128 v[242:245], v130 offset:43008
	v_cvt_pk_f16_f32 v35, v34, v35
	v_cvt_pk_f16_f32 v34, v32, v33
	ds_write_b64 v100, v[34:35] offset:24576
	s_add_u32 s80, s22, 0xc0c00
	s_addc_u32 s81, s90, 0
	global_load_dwordx4 v[88:91], v201, s[80:81] nt
	s_setprio 1
	s_waitcnt lgkmcnt(1)
	v_mfma_f32_16x16x32_f16 v[16:19], v[0:3], v[206:209], v[16:19]
	v_mfma_f32_16x16x32_f16 v[32:35], v[0:3], v[210:213], v[238:241]
	v_mfma_f32_16x16x32_f16 v[170:173], v[0:3], v[214:217], v[170:173]
	v_mfma_f32_16x16x32_f16 v[150:153], v[0:3], v[218:221], v[150:153]
	v_mfma_f32_16x16x32_f16 v[162:165], v[242:245], v[206:209], v[162:165]
	v_mfma_f32_16x16x32_f16 v[174:177], v[242:245], v[210:213], v[174:177]
	v_mfma_f32_16x16x32_f16 v[178:181], v[242:245], v[214:217], v[178:181]
	v_mfma_f32_16x16x32_f16 v[154:157], v[242:245], v[218:221], v[154:157]
	s_setprio 0
	ds_read_b128 v[0:3], v130 offset:45056
	ds_read_b128 v[238:241], v130 offset:47104
	v_cvt_pk_f16_f32 v39, v38, v39
	v_cvt_pk_f16_f32 v38, v36, v37
	ds_write_b64 v100, v[38:39] offset:28672
	s_add_u32 s80, s22, 0xe0c00
	s_addc_u32 s81, s90, 0
	global_load_dwordx4 v[36:39], v201, s[80:81] nt
	s_setprio 1
	s_waitcnt lgkmcnt(1)
	v_mfma_f32_16x16x32_f16 v[20:23], v[0:3], v[206:209], v[20:23]
	v_mfma_f32_16x16x32_f16 v[234:237], v[0:3], v[210:213], v[234:237]
	v_mfma_f32_16x16x32_f16 v[158:161], v[0:3], v[214:217], v[158:161]
	v_mfma_f32_16x16x32_f16 v[166:169], v[0:3], v[218:221], v[166:169]
	v_mfma_f32_16x16x32_f16 v[182:185], v[238:241], v[206:209], v[182:185]
	v_mfma_f32_16x16x32_f16 v[190:193], v[238:241], v[210:213], v[190:193]
	v_mfma_f32_16x16x32_f16 v[202:205], v[238:241], v[214:217], v[202:205]
	v_mfma_f32_16x16x32_f16 v[186:189], v[238:241], v[218:221], v[186:189]
	s_setprio 0
	s_waitcnt vmcnt(4)
	s_waitcnt lgkmcnt(0)
	s_barrier
	ds_read_b128 v[206:209], v131
	ds_read_b128 v[210:213], v131 offset:2048
	ds_read_b128 v[214:217], v131 offset:4096
	ds_read_b128 v[218:221], v131 offset:6144
	ds_read_b128 v[238:241], v129
	ds_read_b128 v[242:245], v129 offset:2048
	s_add_u32 s80, s22, 0xd00
	v_lshl_add_u64 v[92:93], s[48:49], 0, v[196:197]
	s_addc_u32 s81, s90, 0
	s_mov_b32 m0, s0
	v_cvt_pk_f16_f32 v1, v6, v7
	global_load_lds_dwordx4 v[92:93], off
	v_cvt_pk_f16_f32 v0, v4, v5
	ds_write_b64 v100, v[0:1] offset:32768
	global_load_dwordx4 v[0:3], v201, s[80:81] nt
	s_setprio 1
	s_waitcnt lgkmcnt(1)
	v_mfma_f32_16x16x32_f16 v[24:27], v[238:241], v[206:209], v[24:27]
	v_mfma_f32_16x16x32_f16 v[104:107], v[238:241], v[214:217], v[104:107]
	v_mfma_f32_16x16x32_f16 v[108:111], v[242:245], v[206:209], v[108:111]
	v_mfma_f32_16x16x32_f16 v[112:115], v[242:245], v[210:213], v[112:115]
	v_mfma_f32_16x16x32_f16 v[116:119], v[242:245], v[214:217], v[116:119]
	v_mfma_f32_16x16x32_f16 v[230:233], v[238:241], v[210:213], v[230:233]
	v_mfma_f32_16x16x32_f16 v[222:225], v[238:241], v[218:221], v[222:225]
	v_mfma_f32_16x16x32_f16 v[226:229], v[242:245], v[218:221], v[226:229]
	s_setprio 0
	ds_read_b128 v[238:241], v129 offset:4096
	ds_read_b128 v[242:245], v129 offset:6144
	s_mov_b32 m0, s72
	v_lshl_add_u64 v[4:5], v[92:93], 0, s[58:59]
	global_load_lds_dwordx4 v[4:5], off
	v_cvt_pk_f16_f32 v5, v66, v67
	v_cvt_pk_f16_f32 v4, v64, v65
	ds_write_b64 v100, v[4:5] offset:36864
	s_add_u32 s80, s22, 0x20d00
	s_addc_u32 s81, s90, 0
	global_load_dwordx4 v[4:7], v201, s[80:81] nt
	s_setprio 1
	s_waitcnt lgkmcnt(1)
	v_mfma_f32_16x16x32_f16 v[64:67], v[238:241], v[206:209], v[12:15]
	v_mfma_f32_16x16x32_f16 v[28:31], v[238:241], v[210:213], v[28:31]
	v_mfma_f32_16x16x32_f16 v[120:123], v[238:241], v[218:221], v[120:123]
	v_mfma_f32_16x16x32_f16 v[124:127], v[242:245], v[206:209], v[124:127]
	v_mfma_f32_16x16x32_f16 v[146:149], v[242:245], v[214:217], v[146:149]
	v_mfma_f32_16x16x32_f16 v[134:137], v[242:245], v[218:221], v[134:137]
	v_mfma_f32_16x16x32_f16 v[138:141], v[238:241], v[214:217], v[138:141]
	v_mfma_f32_16x16x32_f16 v[142:145], v[242:245], v[210:213], v[142:145]
	s_setprio 0
	ds_read_b128 v[238:241], v129 offset:8192
	ds_read_b128 v[242:245], v129 offset:10240
	s_mov_b32 m0, s71
	v_lshl_add_u64 v[12:13], v[92:93], 0, s[60:61]
	global_load_lds_dwordx4 v[12:13], off
	v_cvt_pk_f16_f32 v13, v42, v43
	v_cvt_pk_f16_f32 v12, v40, v41
	ds_write_b64 v100, v[12:13] offset:40960
	s_add_u32 s80, s22, 0x40d00
	s_addc_u32 s81, s90, 0
	global_load_dwordx4 v[12:15], v201, s[80:81] nt
	s_setprio 1
	s_waitcnt lgkmcnt(1)
	v_mfma_f32_16x16x32_f16 v[40:43], v[238:241], v[206:209], v[16:19]
	v_mfma_f32_16x16x32_f16 v[32:35], v[238:241], v[210:213], v[32:35]
	v_mfma_f32_16x16x32_f16 v[170:173], v[238:241], v[214:217], v[170:173]
	v_mfma_f32_16x16x32_f16 v[150:153], v[238:241], v[218:221], v[150:153]
	v_mfma_f32_16x16x32_f16 v[162:165], v[242:245], v[206:209], v[162:165]
	v_mfma_f32_16x16x32_f16 v[174:177], v[242:245], v[210:213], v[174:177]
	v_mfma_f32_16x16x32_f16 v[178:181], v[242:245], v[214:217], v[178:181]
	v_mfma_f32_16x16x32_f16 v[154:157], v[242:245], v[218:221], v[154:157]
	s_setprio 0
	ds_read_b128 v[238:241], v129 offset:12288
	ds_read_b128 v[242:245], v129 offset:14336
	s_mov_b32 m0, s70
	v_lshl_add_u64 v[16:17], v[92:93], 0, s[62:63]
	global_load_lds_dwordx4 v[16:17], off
	v_cvt_pk_f16_f32 v17, v46, v47
	v_cvt_pk_f16_f32 v16, v44, v45
	ds_write_b64 v100, v[16:17] offset:45056
	s_add_u32 s70, s22, 0x60d00
	s_addc_u32 s71, s90, 0
	global_load_dwordx4 v[16:19], v201, s[70:71] nt
	s_setprio 1
	s_waitcnt lgkmcnt(1)
	v_mfma_f32_16x16x32_f16 v[44:47], v[238:241], v[206:209], v[20:23]
	v_mfma_f32_16x16x32_f16 v[234:237], v[238:241], v[210:213], v[234:237]
	v_mfma_f32_16x16x32_f16 v[158:161], v[238:241], v[214:217], v[158:161]
	v_mfma_f32_16x16x32_f16 v[166:169], v[238:241], v[218:221], v[166:169]
	v_mfma_f32_16x16x32_f16 v[182:185], v[242:245], v[206:209], v[182:185]
	v_mfma_f32_16x16x32_f16 v[190:193], v[242:245], v[210:213], v[190:193]
	v_mfma_f32_16x16x32_f16 v[202:205], v[242:245], v[214:217], v[202:205]
	v_mfma_f32_16x16x32_f16 v[186:189], v[242:245], v[218:221], v[186:189]
	s_setprio 0
	ds_read_b128 v[206:209], v128
	ds_read_b128 v[210:213], v128 offset:2048
	ds_read_b128 v[214:217], v128 offset:4096
	ds_read_b128 v[218:221], v128 offset:6144
	ds_read_b128 v[238:241], v130
	ds_read_b128 v[242:245], v130 offset:2048
	v_cvt_pk_f16_f32 v21, v50, v51
	v_cvt_pk_f16_f32 v20, v48, v49
	ds_write_b64 v100, v[20:21] offset:49152
	s_add_u32 s70, s22, 0x80d00
	s_addc_u32 s71, s90, 0
	global_load_dwordx4 v[20:23], v201, s[70:71] nt
	s_setprio 1
	s_waitcnt lgkmcnt(1)
	v_mfma_f32_16x16x32_f16 v[48:51], v[238:241], v[206:209], v[24:27]
	v_mfma_f32_16x16x32_f16 v[104:107], v[238:241], v[214:217], v[104:107]
	v_mfma_f32_16x16x32_f16 v[108:111], v[242:245], v[206:209], v[108:111]
	v_mfma_f32_16x16x32_f16 v[112:115], v[242:245], v[210:213], v[112:115]
	v_mfma_f32_16x16x32_f16 v[116:119], v[242:245], v[214:217], v[116:119]
	v_mfma_f32_16x16x32_f16 v[230:233], v[238:241], v[210:213], v[230:233]
	v_mfma_f32_16x16x32_f16 v[222:225], v[238:241], v[218:221], v[222:225]
	v_mfma_f32_16x16x32_f16 v[226:229], v[242:245], v[218:221], v[226:229]
	s_setprio 0
	ds_read_b128 v[238:241], v130 offset:4096
	ds_read_b128 v[242:245], v130 offset:6144
	v_cvt_pk_f16_f32 v25, v54, v55
	v_cvt_pk_f16_f32 v24, v52, v53
	ds_write_b64 v100, v[24:25] offset:53248
	s_add_u32 s70, s22, 0xa0d00
	s_addc_u32 s71, s90, 0
	global_load_dwordx4 v[24:27], v201, s[70:71] nt
	s_setprio 1
	s_waitcnt lgkmcnt(1)
	v_mfma_f32_16x16x32_f16 v[52:55], v[238:241], v[206:209], v[64:67]
	v_mfma_f32_16x16x32_f16 v[64:67], v[238:241], v[210:213], v[28:31]
	v_mfma_f32_16x16x32_f16 v[120:123], v[238:241], v[218:221], v[120:123]
	v_mfma_f32_16x16x32_f16 v[124:127], v[242:245], v[206:209], v[124:127]
	v_mfma_f32_16x16x32_f16 v[146:149], v[242:245], v[214:217], v[146:149]
	v_mfma_f32_16x16x32_f16 v[134:137], v[242:245], v[218:221], v[134:137]
	v_mfma_f32_16x16x32_f16 v[138:141], v[238:241], v[214:217], v[138:141]
	v_mfma_f32_16x16x32_f16 v[142:145], v[242:245], v[210:213], v[142:145]
	s_setprio 0
	ds_read_b128 v[238:241], v130 offset:8192
	ds_read_b128 v[242:245], v130 offset:10240
	v_cvt_pk_f16_f32 v29, v58, v59
	v_cvt_pk_f16_f32 v28, v56, v57
	ds_write_b64 v100, v[28:29] offset:57344
	s_add_u32 s70, s22, 0xc0d00
	s_addc_u32 s71, s90, 0
	global_load_dwordx4 v[28:31], v201, s[70:71] nt
	s_setprio 1
	s_waitcnt lgkmcnt(1)
	v_mfma_f32_16x16x32_f16 v[56:59], v[238:241], v[206:209], v[40:43]
	v_mfma_f32_16x16x32_f16 v[246:249], v[238:241], v[210:213], v[32:35]
	v_mfma_f32_16x16x32_f16 v[170:173], v[238:241], v[214:217], v[170:173]
	v_mfma_f32_16x16x32_f16 v[150:153], v[238:241], v[218:221], v[150:153]
	v_mfma_f32_16x16x32_f16 v[162:165], v[242:245], v[206:209], v[162:165]
	v_mfma_f32_16x16x32_f16 v[174:177], v[242:245], v[210:213], v[174:177]
	v_mfma_f32_16x16x32_f16 v[178:181], v[242:245], v[214:217], v[178:181]
	v_mfma_f32_16x16x32_f16 v[154:157], v[242:245], v[218:221], v[154:157]
	s_setprio 0
	ds_read_b128 v[40:43], v130 offset:12288
	ds_read_b128 v[238:241], v130 offset:14336
	v_cvt_pk_f16_f32 v33, v62, v63
	v_cvt_pk_f16_f32 v32, v60, v61
	ds_write_b64 v100, v[32:33] offset:61440
	s_add_u32 s70, s22, 0xe0d00
	s_addc_u32 s71, s90, 0
	global_load_dwordx4 v[32:35], v201, s[70:71] nt
	s_setprio 1
	s_waitcnt lgkmcnt(1)
	v_mfma_f32_16x16x32_f16 v[60:63], v[40:43], v[206:209], v[44:47]
	v_mfma_f32_16x16x32_f16 v[234:237], v[40:43], v[210:213], v[234:237]
	v_mfma_f32_16x16x32_f16 v[158:161], v[40:43], v[214:217], v[158:161]
	v_mfma_f32_16x16x32_f16 v[166:169], v[40:43], v[218:221], v[166:169]
	v_mfma_f32_16x16x32_f16 v[182:185], v[238:241], v[206:209], v[182:185]
	v_mfma_f32_16x16x32_f16 v[190:193], v[238:241], v[210:213], v[190:193]
	v_mfma_f32_16x16x32_f16 v[202:205], v[238:241], v[214:217], v[202:205]
	v_mfma_f32_16x16x32_f16 v[186:189], v[238:241], v[218:221], v[186:189]
	s_setprio 0
	s_waitcnt vmcnt(4)
	s_waitcnt lgkmcnt(0)
	s_barrier
	ds_read_b128 v[206:209], v131 offset:32768
	ds_read_b128 v[210:213], v131 offset:34816
	ds_read_b128 v[214:217], v131 offset:36864
	ds_read_b128 v[218:221], v131 offset:38912
	ds_read_b128 v[40:43], v129 offset:32768
	ds_read_b128 v[44:47], v129 offset:34816
	s_add_u32 s70, s22, 0xe00
	v_lshl_add_u64 v[92:93], s[50:51], 0, v[196:197]
	s_addc_u32 s71, s90, 0
	s_mov_b32 m0, s1
	v_cvt_pk_f16_f32 v11, v10, v11
	global_load_lds_dwordx4 v[92:93], off
	v_cvt_pk_f16_f32 v10, v8, v9
	ds_write_b64 v100, v[10:11]
	global_load_dwordx4 v[8:11], v201, s[70:71] nt
	s_setprio 1
	s_waitcnt lgkmcnt(1)
	v_mfma_f32_16x16x32_f16 v[104:107], v[40:43], v[214:217], v[104:107]
	v_mfma_f32_16x16x32_f16 v[108:111], v[44:47], v[206:209], v[108:111]
	v_mfma_f32_16x16x32_f16 v[112:115], v[44:47], v[210:213], v[112:115]
	v_mfma_f32_16x16x32_f16 v[116:119], v[44:47], v[214:217], v[116:119]
	v_mfma_f32_16x16x32_f16 v[238:241], v[40:43], v[206:209], v[48:51]
	v_mfma_f32_16x16x32_f16 v[230:233], v[40:43], v[210:213], v[230:233]
	v_mfma_f32_16x16x32_f16 v[222:225], v[40:43], v[218:221], v[222:225]
	v_mfma_f32_16x16x32_f16 v[226:229], v[44:47], v[218:221], v[226:229]
	s_setprio 0
	ds_read_b128 v[44:47], v129 offset:36864
	ds_read_b128 v[48:51], v129 offset:38912
	s_mov_b32 m0, s92
	v_lshl_add_u64 v[40:41], v[92:93], 0, s[58:59]
	global_load_lds_dwordx4 v[40:41], off
	v_cvt_pk_f16_f32 v41, v70, v71
	v_cvt_pk_f16_f32 v40, v68, v69
	ds_write_b64 v100, v[40:41] offset:4096
	s_add_u32 s0, s22, 0x20e00
	s_addc_u32 s1, s90, 0
	global_load_dwordx4 v[40:43], v201, s[0:1] nt
	s_setprio 1
	s_waitcnt lgkmcnt(1)
	v_mfma_f32_16x16x32_f16 v[68:71], v[44:47], v[206:209], v[52:55]
	v_mfma_f32_16x16x32_f16 v[64:67], v[44:47], v[210:213], v[64:67]
	v_mfma_f32_16x16x32_f16 v[120:123], v[44:47], v[218:221], v[120:123]
	v_mfma_f32_16x16x32_f16 v[124:127], v[48:51], v[206:209], v[124:127]
	v_mfma_f32_16x16x32_f16 v[146:149], v[48:51], v[214:217], v[146:149]
	v_mfma_f32_16x16x32_f16 v[134:137], v[48:51], v[218:221], v[134:137]
	v_mfma_f32_16x16x32_f16 v[138:141], v[44:47], v[214:217], v[138:141]
	v_mfma_f32_16x16x32_f16 v[142:145], v[48:51], v[210:213], v[142:145]
	s_setprio 0
	ds_read_b128 v[48:51], v129 offset:40960
	ds_read_b128 v[52:55], v129 offset:43008
	s_mov_b32 m0, s91
	v_lshl_add_u64 v[44:45], v[92:93], 0, s[60:61]
	global_load_lds_dwordx4 v[44:45], off
	v_cvt_pk_f16_f32 v45, v74, v75
	v_cvt_pk_f16_f32 v44, v72, v73
	ds_write_b64 v100, v[44:45] offset:8192
	s_add_u32 s0, s22, 0x40e00
	s_addc_u32 s1, s90, 0
	global_load_dwordx4 v[44:47], v201, s[0:1] nt
	s_setprio 1
	s_waitcnt lgkmcnt(1)
	v_mfma_f32_16x16x32_f16 v[72:75], v[48:51], v[206:209], v[56:59]
	v_mfma_f32_16x16x32_f16 v[242:245], v[48:51], v[210:213], v[246:249]
	v_mfma_f32_16x16x32_f16 v[170:173], v[48:51], v[214:217], v[170:173]
	v_mfma_f32_16x16x32_f16 v[150:153], v[48:51], v[218:221], v[150:153]
	v_mfma_f32_16x16x32_f16 v[162:165], v[52:55], v[206:209], v[162:165]
	v_mfma_f32_16x16x32_f16 v[174:177], v[52:55], v[210:213], v[174:177]
	v_mfma_f32_16x16x32_f16 v[178:181], v[52:55], v[214:217], v[178:181]
	v_mfma_f32_16x16x32_f16 v[154:157], v[52:55], v[218:221], v[154:157]
	s_setprio 0
	ds_read_b128 v[52:55], v129 offset:45056
	ds_read_b128 v[56:59], v129 offset:47104
	s_mov_b32 m0, s73
	v_lshl_add_u64 v[48:49], v[92:93], 0, s[62:63]
	global_load_lds_dwordx4 v[48:49], off
	v_cvt_pk_f16_f32 v49, v78, v79
	v_cvt_pk_f16_f32 v48, v76, v77
	ds_write_b64 v100, v[48:49] offset:12288
	s_add_u32 s0, s22, 0x60e00
	s_addc_u32 s1, s90, 0
	global_load_dwordx4 v[48:51], v201, s[0:1] nt
	s_setprio 1
	s_waitcnt lgkmcnt(1)
	v_mfma_f32_16x16x32_f16 v[76:79], v[52:55], v[206:209], v[60:63]
	v_mfma_f32_16x16x32_f16 v[234:237], v[52:55], v[210:213], v[234:237]
	v_mfma_f32_16x16x32_f16 v[158:161], v[52:55], v[214:217], v[158:161]
	v_mfma_f32_16x16x32_f16 v[166:169], v[52:55], v[218:221], v[166:169]
	v_mfma_f32_16x16x32_f16 v[182:185], v[56:59], v[206:209], v[182:185]
	v_mfma_f32_16x16x32_f16 v[190:193], v[56:59], v[210:213], v[190:193]
	v_mfma_f32_16x16x32_f16 v[202:205], v[56:59], v[214:217], v[202:205]
	v_mfma_f32_16x16x32_f16 v[186:189], v[56:59], v[218:221], v[186:189]
	s_setprio 0
	ds_read_b128 v[206:209], v128 offset:32768
	ds_read_b128 v[210:213], v128 offset:34816
	ds_read_b128 v[214:217], v128 offset:36864
	ds_read_b128 v[218:221], v128 offset:38912
	ds_read_b128 v[56:59], v130 offset:32768
	ds_read_b128 v[60:63], v130 offset:34816
	v_cvt_pk_f16_f32 v53, v82, v83
	v_cvt_pk_f16_f32 v52, v80, v81
	ds_write_b64 v100, v[52:53] offset:16384
	s_add_u32 s0, s22, 0x80e00
	s_addc_u32 s1, s90, 0
	global_load_dwordx4 v[52:55], v201, s[0:1] nt
	s_setprio 1
	s_waitcnt lgkmcnt(1)
	v_mfma_f32_16x16x32_f16 v[80:83], v[56:59], v[206:209], v[238:241]
	v_mfma_f32_16x16x32_f16 v[104:107], v[56:59], v[214:217], v[104:107]
	v_mfma_f32_16x16x32_f16 v[108:111], v[60:63], v[206:209], v[108:111]
	v_mfma_f32_16x16x32_f16 v[112:115], v[60:63], v[210:213], v[112:115]
	v_mfma_f32_16x16x32_f16 v[116:119], v[60:63], v[214:217], v[116:119]
	v_mfma_f32_16x16x32_f16 v[230:233], v[56:59], v[210:213], v[230:233]
	v_mfma_f32_16x16x32_f16 v[222:225], v[56:59], v[218:221], v[222:225]
	v_mfma_f32_16x16x32_f16 v[226:229], v[60:63], v[218:221], v[226:229]
	s_setprio 0
	ds_read_b128 v[60:63], v130 offset:36864
	ds_read_b128 v[238:241], v130 offset:38912
	v_cvt_pk_f16_f32 v57, v86, v87
	v_cvt_pk_f16_f32 v56, v84, v85
	ds_write_b64 v100, v[56:57] offset:20480
	s_add_u32 s0, s22, 0xa0e00
	s_addc_u32 s1, s90, 0
	global_load_dwordx4 v[56:59], v201, s[0:1] nt
	s_setprio 1
	s_waitcnt lgkmcnt(1)
	v_mfma_f32_16x16x32_f16 v[68:71], v[60:63], v[206:209], v[68:71]
	v_mfma_f32_16x16x32_f16 v[64:67], v[60:63], v[210:213], v[64:67]
	v_mfma_f32_16x16x32_f16 v[84:87], v[60:63], v[214:217], v[138:141]
	v_mfma_f32_16x16x32_f16 v[120:123], v[60:63], v[218:221], v[120:123]
	v_mfma_f32_16x16x32_f16 v[124:127], v[238:241], v[206:209], v[124:127]
	v_mfma_f32_16x16x32_f16 v[134:137], v[238:241], v[218:221], v[134:137]
	v_mfma_f32_16x16x32_f16 v[138:141], v[238:241], v[210:213], v[142:145]
	v_mfma_f32_16x16x32_f16 v[142:145], v[238:241], v[214:217], v[146:149]
	s_setprio 0
	s_nop 1
	ds_read_b128 v[146:149], v130 offset:40960
	ds_read_b128 v[238:241], v130 offset:43008
	v_cvt_pk_f16_f32 v61, v90, v91
	v_cvt_pk_f16_f32 v60, v88, v89
	ds_write_b64 v100, v[60:61] offset:24576
	s_add_u32 s0, s22, 0xc0e00
	s_addc_u32 s1, s90, 0
	global_load_dwordx4 v[60:63], v201, s[0:1] nt
	s_setprio 1
	s_waitcnt lgkmcnt(1)
	v_mfma_f32_16x16x32_f16 v[72:75], v[146:149], v[206:209], v[72:75]
	v_mfma_f32_16x16x32_f16 v[88:91], v[146:149], v[210:213], v[242:245]
	v_mfma_f32_16x16x32_f16 v[170:173], v[146:149], v[214:217], v[170:173]
	v_mfma_f32_16x16x32_f16 v[146:149], v[146:149], v[218:221], v[150:153]
	v_mfma_f32_16x16x32_f16 v[150:153], v[238:241], v[206:209], v[162:165]
	v_mfma_f32_16x16x32_f16 v[162:165], v[238:241], v[210:213], v[174:177]
	v_mfma_f32_16x16x32_f16 v[174:177], v[238:241], v[214:217], v[178:181]
	v_mfma_f32_16x16x32_f16 v[154:157], v[238:241], v[218:221], v[154:157]
	s_setprio 0
	s_nop 0
	ds_read_b128 v[178:181], v130 offset:45056
	ds_read_b128 v[238:241], v130 offset:47104
	v_cvt_pk_f16_f32 v39, v38, v39
	v_cvt_pk_f16_f32 v38, v36, v37
	ds_write_b64 v100, v[38:39] offset:28672
	s_add_u32 s0, s22, 0xe0e00
	s_addc_u32 s1, s90, 0
	global_load_dwordx4 v[36:39], v201, s[0:1] nt
	s_setprio 1
	s_waitcnt lgkmcnt(1)
	v_mfma_f32_16x16x32_f16 v[76:79], v[178:181], v[206:209], v[76:79]
	v_mfma_f32_16x16x32_f16 v[234:237], v[178:181], v[210:213], v[234:237]
	v_mfma_f32_16x16x32_f16 v[158:161], v[178:181], v[214:217], v[158:161]
	v_mfma_f32_16x16x32_f16 v[166:169], v[178:181], v[218:221], v[166:169]
	v_mfma_f32_16x16x32_f16 v[178:181], v[238:241], v[206:209], v[182:185]
	v_mfma_f32_16x16x32_f16 v[182:185], v[238:241], v[210:213], v[190:193]
	v_mfma_f32_16x16x32_f16 v[190:193], v[238:241], v[214:217], v[202:205]
	v_mfma_f32_16x16x32_f16 v[186:189], v[238:241], v[218:221], v[186:189]
	s_setprio 0
	s_waitcnt vmcnt(4)
	s_waitcnt lgkmcnt(0)
	s_barrier
	ds_read_b128 v[202:205], v131
	ds_read_b128 v[206:209], v131 offset:2048
	ds_read_b128 v[210:213], v131 offset:4096
	ds_read_b128 v[214:217], v131 offset:6144
	ds_read_b128 v[218:221], v129
	ds_read_b128 v[238:241], v129 offset:2048
	s_add_u32 s70, s22, 0xf00
	v_lshl_add_u64 v[92:93], s[52:53], 0, v[196:197]
	s_addc_u32 s71, s90, 0
	v_readfirstlane_b32 s0, v95
	s_mov_b32 m0, s0
	v_cvt_pk_f16_f32 v3, v2, v3
	global_load_lds_dwordx4 v[92:93], off
	v_cvt_pk_f16_f32 v2, v0, v1
	ds_write_b64 v100, v[2:3] offset:32768
	global_load_dwordx4 v[0:3], v201, s[70:71] nt
	s_setprio 1
	s_waitcnt lgkmcnt(1)
	v_mfma_f32_16x16x32_f16 v[80:83], v[218:221], v[202:205], v[80:83]
	v_mfma_f32_16x16x32_f16 v[104:107], v[218:221], v[210:213], v[104:107]
	v_mfma_f32_16x16x32_f16 v[108:111], v[238:241], v[202:205], v[108:111]
	v_mfma_f32_16x16x32_f16 v[112:115], v[238:241], v[206:209], v[112:115]
	v_mfma_f32_16x16x32_f16 v[116:119], v[238:241], v[210:213], v[116:119]
	v_mfma_f32_16x16x32_f16 v[230:233], v[218:221], v[206:209], v[230:233]
	v_mfma_f32_16x16x32_f16 v[218:221], v[218:221], v[214:217], v[222:225]
	v_mfma_f32_16x16x32_f16 v[222:225], v[238:241], v[214:217], v[226:229]
	s_setprio 0
	s_nop 1
	ds_read_b128 v[226:229], v129 offset:4096
	ds_read_b128 v[238:241], v129 offset:6144
	v_readfirstlane_b32 s1, v96
	v_lshl_add_u64 v[198:199], v[92:93], 0, s[58:59]
	s_mov_b32 m0, s1
	v_cvt_pk_f16_f32 v7, v6, v7
	global_load_lds_dwordx4 v[198:199], off
	v_cvt_pk_f16_f32 v6, v4, v5
	ds_write_b64 v100, v[6:7] offset:36864
	s_add_u32 s70, s22, 0x20f00
	s_addc_u32 s71, s90, 0
	global_load_dwordx4 v[4:7], v201, s[70:71] nt
	s_setprio 1
	s_waitcnt lgkmcnt(1)
	v_mfma_f32_16x16x32_f16 v[68:71], v[226:229], v[202:205], v[68:71]
	v_mfma_f32_16x16x32_f16 v[64:67], v[226:229], v[206:209], v[64:67]
	v_mfma_f32_16x16x32_f16 v[84:87], v[226:229], v[210:213], v[84:87]
	v_mfma_f32_16x16x32_f16 v[120:123], v[226:229], v[214:217], v[120:123]
	v_mfma_f32_16x16x32_f16 v[124:127], v[238:241], v[202:205], v[124:127]
	v_mfma_f32_16x16x32_f16 v[134:137], v[238:241], v[214:217], v[134:137]
	v_mfma_f32_16x16x32_f16 v[138:141], v[238:241], v[206:209], v[138:141]
	v_mfma_f32_16x16x32_f16 v[142:145], v[238:241], v[210:213], v[142:145]
	s_setprio 0
	ds_read_b128 v[226:229], v129 offset:8192
	ds_read_b128 v[238:241], v129 offset:10240
	v_readfirstlane_b32 s70, v97
	v_lshl_add_u64 v[198:199], v[92:93], 0, s[60:61]
	s_mov_b32 m0, s70
	v_cvt_pk_f16_f32 v15, v14, v15
	global_load_lds_dwordx4 v[198:199], off
	v_cvt_pk_f16_f32 v14, v12, v13
	ds_write_b64 v100, v[14:15] offset:40960
	s_add_u32 s72, s22, 0x40f00
	s_addc_u32 s73, s90, 0
	global_load_dwordx4 v[12:15], v201, s[72:73] nt
	s_setprio 1
	s_waitcnt lgkmcnt(1)
	v_mfma_f32_16x16x32_f16 v[72:75], v[226:229], v[202:205], v[72:75]
	v_mfma_f32_16x16x32_f16 v[88:91], v[226:229], v[206:209], v[88:91]
	v_mfma_f32_16x16x32_f16 v[146:149], v[226:229], v[214:217], v[146:149]
	v_mfma_f32_16x16x32_f16 v[170:173], v[226:229], v[210:213], v[170:173]
	v_mfma_f32_16x16x32_f16 v[150:153], v[238:241], v[202:205], v[150:153]
	v_mfma_f32_16x16x32_f16 v[162:165], v[238:241], v[206:209], v[162:165]
	v_mfma_f32_16x16x32_f16 v[174:177], v[238:241], v[210:213], v[174:177]
	v_mfma_f32_16x16x32_f16 v[154:157], v[238:241], v[214:217], v[154:157]
	s_setprio 0
	ds_read_b128 v[226:229], v129 offset:12288
	ds_read_b128 v[238:241], v129 offset:14336
	v_readfirstlane_b32 s71, v98
	v_lshl_add_u64 v[92:93], v[92:93], 0, s[62:63]
	s_mov_b32 m0, s71
	v_cvt_pk_f16_f32 v19, v18, v19
	global_load_lds_dwordx4 v[92:93], off
	v_cvt_pk_f16_f32 v18, v16, v17
	ds_write_b64 v100, v[18:19] offset:45056
	s_add_u32 s72, s22, 0x60f00
	s_addc_u32 s73, s90, 0
	global_load_dwordx4 v[16:19], v201, s[72:73] nt
	s_setprio 1
	s_waitcnt lgkmcnt(1)
	v_mfma_f32_16x16x32_f16 v[76:79], v[226:229], v[202:205], v[76:79]
	v_mfma_f32_16x16x32_f16 v[234:237], v[226:229], v[206:209], v[234:237]
	v_mfma_f32_16x16x32_f16 v[158:161], v[226:229], v[210:213], v[158:161]
	v_mfma_f32_16x16x32_f16 v[166:169], v[226:229], v[214:217], v[166:169]
	v_mfma_f32_16x16x32_f16 v[178:181], v[238:241], v[202:205], v[178:181]
	v_mfma_f32_16x16x32_f16 v[182:185], v[238:241], v[206:209], v[182:185]
	v_mfma_f32_16x16x32_f16 v[190:193], v[238:241], v[210:213], v[190:193]
	v_mfma_f32_16x16x32_f16 v[186:189], v[238:241], v[214:217], v[186:189]
	s_setprio 0
	ds_read_b128 v[202:205], v128
	ds_read_b128 v[206:209], v128 offset:2048
	ds_read_b128 v[210:213], v128 offset:4096
	ds_read_b128 v[214:217], v128 offset:6144
	ds_read_b128 v[226:229], v130
	ds_read_b128 v[238:241], v130 offset:2048
	v_cvt_pk_f16_f32 v23, v22, v23
	v_cvt_pk_f16_f32 v22, v20, v21
	ds_write_b64 v100, v[22:23] offset:49152
	s_add_u32 s72, s22, 0x80f00
	s_addc_u32 s73, s90, 0
	global_load_dwordx4 v[20:23], v201, s[72:73] nt
	s_setprio 1
	s_waitcnt lgkmcnt(1)
	v_mfma_f32_16x16x32_f16 v[80:83], v[226:229], v[202:205], v[80:83]
	v_mfma_f32_16x16x32_f16 v[104:107], v[226:229], v[210:213], v[104:107]
	v_mfma_f32_16x16x32_f16 v[108:111], v[238:241], v[202:205], v[108:111]
	v_mfma_f32_16x16x32_f16 v[112:115], v[238:241], v[206:209], v[112:115]
	v_mfma_f32_16x16x32_f16 v[116:119], v[238:241], v[210:213], v[116:119]
	v_mfma_f32_16x16x32_f16 v[230:233], v[226:229], v[206:209], v[230:233]
	v_mfma_f32_16x16x32_f16 v[218:221], v[226:229], v[214:217], v[218:221]
	v_mfma_f32_16x16x32_f16 v[222:225], v[238:241], v[214:217], v[222:225]
	s_setprio 0
	ds_read_b128 v[226:229], v130 offset:4096
	ds_read_b128 v[238:241], v130 offset:6144
	v_cvt_pk_f16_f32 v27, v26, v27
	v_cvt_pk_f16_f32 v26, v24, v25
	ds_write_b64 v100, v[26:27] offset:53248
	s_add_u32 s72, s22, 0xa0f00
	s_addc_u32 s73, s90, 0
	global_load_dwordx4 v[24:27], v201, s[72:73] nt
	s_setprio 1
	s_waitcnt lgkmcnt(1)
	v_mfma_f32_16x16x32_f16 v[68:71], v[226:229], v[202:205], v[68:71]
	v_mfma_f32_16x16x32_f16 v[64:67], v[226:229], v[206:209], v[64:67]
	v_mfma_f32_16x16x32_f16 v[84:87], v[226:229], v[210:213], v[84:87]
	v_mfma_f32_16x16x32_f16 v[120:123], v[226:229], v[214:217], v[120:123]
	v_mfma_f32_16x16x32_f16 v[124:127], v[238:241], v[202:205], v[124:127]
	v_mfma_f32_16x16x32_f16 v[134:137], v[238:241], v[214:217], v[134:137]
	v_mfma_f32_16x16x32_f16 v[138:141], v[238:241], v[206:209], v[138:141]
	v_mfma_f32_16x16x32_f16 v[142:145], v[238:241], v[210:213], v[142:145]
	s_setprio 0
	ds_read_b128 v[226:229], v130 offset:8192
	ds_read_b128 v[238:241], v130 offset:10240
	v_cvt_pk_f16_f32 v31, v30, v31
	v_cvt_pk_f16_f32 v30, v28, v29
	ds_write_b64 v100, v[30:31] offset:57344
	s_add_u32 s72, s22, 0xc0f00
	s_addc_u32 s73, s90, 0
	global_load_dwordx4 v[28:31], v201, s[72:73] nt
	s_setprio 1
	s_waitcnt lgkmcnt(1)
	v_mfma_f32_16x16x32_f16 v[72:75], v[226:229], v[202:205], v[72:75]
	v_mfma_f32_16x16x32_f16 v[88:91], v[226:229], v[206:209], v[88:91]
	v_mfma_f32_16x16x32_f16 v[146:149], v[226:229], v[214:217], v[146:149]
	v_mfma_f32_16x16x32_f16 v[170:173], v[226:229], v[210:213], v[170:173]
	v_mfma_f32_16x16x32_f16 v[150:153], v[238:241], v[202:205], v[150:153]
	v_mfma_f32_16x16x32_f16 v[162:165], v[238:241], v[206:209], v[162:165]
	v_mfma_f32_16x16x32_f16 v[174:177], v[238:241], v[210:213], v[174:177]
	v_mfma_f32_16x16x32_f16 v[154:157], v[238:241], v[214:217], v[154:157]
	s_setprio 0
	ds_read_b128 v[226:229], v130 offset:12288
	ds_read_b128 v[238:241], v130 offset:14336
	v_cvt_pk_f16_f32 v35, v34, v35
	v_cvt_pk_f16_f32 v34, v32, v33
	ds_write_b64 v100, v[34:35] offset:61440
	s_add_u32 s72, s22, 0xe0f00
	s_addc_u32 s73, s90, 0
	global_load_dwordx4 v[32:35], v201, s[72:73] nt
	s_setprio 1
	s_waitcnt lgkmcnt(1)
	v_mfma_f32_16x16x32_f16 v[76:79], v[226:229], v[202:205], v[76:79]
	v_mfma_f32_16x16x32_f16 v[234:237], v[226:229], v[206:209], v[234:237]
	v_mfma_f32_16x16x32_f16 v[158:161], v[226:229], v[210:213], v[158:161]
	v_mfma_f32_16x16x32_f16 v[166:169], v[226:229], v[214:217], v[166:169]
	v_mfma_f32_16x16x32_f16 v[178:181], v[238:241], v[202:205], v[178:181]
	v_mfma_f32_16x16x32_f16 v[182:185], v[238:241], v[206:209], v[182:185]
	v_mfma_f32_16x16x32_f16 v[190:193], v[238:241], v[210:213], v[190:193]
	v_mfma_f32_16x16x32_f16 v[186:189], v[238:241], v[214:217], v[186:189]
	s_setprio 0
	s_waitcnt vmcnt(4)
	s_waitcnt lgkmcnt(0)
	s_barrier
	ds_read_b128 v[202:205], v131 offset:32768
	ds_read_b128 v[206:209], v131 offset:34816
	ds_read_b128 v[210:213], v131 offset:36864
	ds_read_b128 v[214:217], v131 offset:38912
	ds_read_b128 v[226:229], v129 offset:32768
	ds_read_b128 v[238:241], v129 offset:34816
	v_lshl_add_u64 v[198:199], s[54:55], 0, v[196:197]
	v_readfirstlane_b32 s64, v94
	s_mov_b32 m0, s64
	v_cvt_pk_f16_f32 v11, v10, v11
	global_load_lds_dwordx4 v[198:199], off
	v_cvt_pk_f16_f32 v10, v8, v9
	ds_write_b64 v100, v[10:11]
	s_setprio 1
	s_waitcnt lgkmcnt(1)
	v_mfma_f32_16x16x32_f16 v[8:11], v[226:229], v[202:205], v[80:83]
	v_mfma_f32_16x16x32_f16 v[80:83], v[226:229], v[206:209], v[230:233]
	v_mfma_f32_16x16x32_f16 v[92:95], v[226:229], v[210:213], v[104:107]
	v_mfma_f32_16x16x32_f16 v[104:107], v[226:229], v[214:217], v[218:221]
	v_mfma_f32_16x16x32_f16 v[108:111], v[238:241], v[202:205], v[108:111]
	v_mfma_f32_16x16x32_f16 v[112:115], v[238:241], v[206:209], v[112:115]
	v_mfma_f32_16x16x32_f16 v[116:119], v[238:241], v[210:213], v[116:119]
	v_mfma_f32_16x16x32_f16 v[218:221], v[238:241], v[214:217], v[222:225]
	s_setprio 0
	s_nop 1
	ds_read_b128 v[222:225], v129 offset:36864
	ds_read_b128 v[226:229], v129 offset:38912
	v_readfirstlane_b32 s64, v99
	v_lshl_add_u64 v[96:97], v[198:199], 0, s[58:59]
	s_mov_b32 m0, s64
	v_cvt_pk_f16_f32 v43, v42, v43
	global_load_lds_dwordx4 v[96:97], off
	v_cvt_pk_f16_f32 v42, v40, v41
	ds_write_b64 v100, v[42:43] offset:4096
	s_setprio 1
	s_waitcnt lgkmcnt(1)
	v_mfma_f32_16x16x32_f16 v[40:43], v[222:225], v[202:205], v[68:71]
	v_mfma_f32_16x16x32_f16 v[64:67], v[222:225], v[206:209], v[64:67]
	v_mfma_f32_16x16x32_f16 v[68:71], v[222:225], v[210:213], v[84:87]
	v_mfma_f32_16x16x32_f16 v[84:87], v[222:225], v[214:217], v[120:123]
	v_mfma_f32_16x16x32_f16 v[96:99], v[226:229], v[202:205], v[124:127]
	v_mfma_f32_16x16x32_f16 v[120:123], v[226:229], v[206:209], v[138:141]
	v_mfma_f32_16x16x32_f16 v[124:127], v[226:229], v[210:213], v[142:145]
	v_mfma_f32_16x16x32_f16 v[134:137], v[226:229], v[214:217], v[134:137]
	s_setprio 0
	ds_read_b128 v[138:141], v129 offset:40960
	ds_read_b128 v[142:145], v129 offset:43008
	v_readfirstlane_b32 s64, v101
	v_lshl_add_u64 v[222:223], v[198:199], 0, s[60:61]
	s_mov_b32 m0, s64
	v_cvt_pk_f16_f32 v47, v46, v47
	global_load_lds_dwordx4 v[222:223], off
	v_cvt_pk_f16_f32 v46, v44, v45
	ds_write_b64 v100, v[46:47] offset:8192
	s_setprio 1
	s_waitcnt lgkmcnt(1)
	v_mfma_f32_16x16x32_f16 v[44:47], v[138:141], v[202:205], v[72:75]
	v_mfma_f32_16x16x32_f16 v[72:75], v[138:141], v[206:209], v[88:91]
	v_mfma_f32_16x16x32_f16 v[88:91], v[138:141], v[210:213], v[170:173]
	v_mfma_f32_16x16x32_f16 v[138:141], v[138:141], v[214:217], v[146:149]
	v_mfma_f32_16x16x32_f16 v[146:149], v[142:145], v[202:205], v[150:153]
	v_mfma_f32_16x16x32_f16 v[150:153], v[142:145], v[206:209], v[162:165]
	v_mfma_f32_16x16x32_f16 v[162:165], v[142:145], v[210:213], v[174:177]
	v_mfma_f32_16x16x32_f16 v[142:145], v[142:145], v[214:217], v[154:157]
	s_setprio 0
	s_nop 1
	ds_read_b128 v[154:157], v129 offset:45056
	ds_read_b128 v[170:173], v129 offset:47104
	v_readfirstlane_b32 s64, v102
	v_lshl_add_u64 v[174:175], v[198:199], 0, s[62:63]
	s_mov_b32 m0, s64
	v_cvt_pk_f16_f32 v51, v50, v51
	global_load_lds_dwordx4 v[174:175], off
	v_cvt_pk_f16_f32 v50, v48, v49
	ds_write_b64 v100, v[50:51] offset:12288
	s_setprio 1
	s_waitcnt lgkmcnt(1)
	v_mfma_f32_16x16x32_f16 v[48:51], v[154:157], v[202:205], v[76:79]
	v_mfma_f32_16x16x32_f16 v[76:79], v[154:157], v[206:209], v[234:237]
	v_mfma_f32_16x16x32_f16 v[158:161], v[154:157], v[210:213], v[158:161]
	v_mfma_f32_16x16x32_f16 v[154:157], v[154:157], v[214:217], v[166:169]
	v_mfma_f32_16x16x32_f16 v[166:169], v[170:173], v[202:205], v[178:181]
	v_mfma_f32_16x16x32_f16 v[174:177], v[170:173], v[206:209], v[182:185]
	v_mfma_f32_16x16x32_f16 v[178:181], v[170:173], v[210:213], v[190:193]
	v_mfma_f32_16x16x32_f16 v[170:173], v[170:173], v[214:217], v[186:189]
	s_setprio 0
	ds_read_b128 v[182:185], v128 offset:32768
	s_nop 0
	ds_read_b128 v[186:189], v128 offset:34816
	ds_read_b128 v[190:193], v128 offset:36864
	ds_read_b128 v[202:205], v128 offset:38912
	ds_read_b128 v[206:209], v130 offset:32768
	ds_read_b128 v[210:213], v130 offset:34816
	v_cvt_pk_f16_f32 v55, v54, v55
	v_cvt_pk_f16_f32 v54, v52, v53
	ds_write_b64 v100, v[54:55] offset:16384
	s_setprio 1
	s_waitcnt lgkmcnt(1)
	v_mfma_f32_16x16x32_f16 v[8:11], v[206:209], v[182:185], v[8:11]
	v_mfma_f32_16x16x32_f16 v[52:55], v[206:209], v[186:189], v[80:83]
	v_mfma_f32_16x16x32_f16 v[80:83], v[206:209], v[190:193], v[92:95]
	v_mfma_f32_16x16x32_f16 v[92:95], v[206:209], v[202:205], v[104:107]
	v_mfma_f32_16x16x32_f16 v[102:105], v[210:213], v[182:185], v[108:111]
	v_mfma_f32_16x16x32_f16 v[106:109], v[210:213], v[186:189], v[112:115]
	v_mfma_f32_16x16x32_f16 v[110:113], v[210:213], v[190:193], v[116:119]
	v_mfma_f32_16x16x32_f16 v[114:117], v[210:213], v[202:205], v[218:221]
	s_setprio 0
	ds_read_b128 v[206:209], v130 offset:36864
	ds_read_b128 v[210:213], v130 offset:38912
	v_cvt_pk_f16_f32 v59, v58, v59
	v_cvt_pk_f16_f32 v58, v56, v57
	ds_write_b64 v100, v[58:59] offset:20480
	s_setprio 1
	s_waitcnt lgkmcnt(1)
	v_mfma_f32_16x16x32_f16 v[40:43], v[206:209], v[182:185], v[40:43]
	v_mfma_f32_16x16x32_f16 v[56:59], v[206:209], v[186:189], v[64:67]
	v_mfma_f32_16x16x32_f16 v[64:67], v[206:209], v[190:193], v[68:71]
	v_mfma_f32_16x16x32_f16 v[68:71], v[206:209], v[202:205], v[84:87]
	v_mfma_f32_16x16x32_f16 v[84:87], v[210:213], v[182:185], v[96:99]
	v_mfma_f32_16x16x32_f16 v[96:99], v[210:213], v[186:189], v[120:123]
	v_mfma_f32_16x16x32_f16 v[118:121], v[210:213], v[190:193], v[124:127]
	v_mfma_f32_16x16x32_f16 v[122:125], v[210:213], v[202:205], v[134:137]
	s_setprio 0
	s_nop 1
	ds_read_b128 v[134:137], v130 offset:40960
	ds_read_b128 v[206:209], v130 offset:43008
	v_cvt_pk_f16_f32 v63, v62, v63
	v_cvt_pk_f16_f32 v62, v60, v61
	ds_write_b64 v100, v[62:63] offset:24576
	s_setprio 1
	s_waitcnt lgkmcnt(1)
	v_mfma_f32_16x16x32_f16 v[44:47], v[134:137], v[182:185], v[44:47]
	v_mfma_f32_16x16x32_f16 v[60:63], v[134:137], v[186:189], v[72:75]
	v_mfma_f32_16x16x32_f16 v[72:75], v[134:137], v[190:193], v[88:91]
	v_mfma_f32_16x16x32_f16 v[88:91], v[134:137], v[202:205], v[138:141]
	v_mfma_f32_16x16x32_f16 v[134:137], v[206:209], v[182:185], v[146:149]
	v_mfma_f32_16x16x32_f16 v[146:149], v[206:209], v[190:193], v[162:165]
	v_mfma_f32_16x16x32_f16 v[138:141], v[206:209], v[186:189], v[150:153]
	v_mfma_f32_16x16x32_f16 v[142:145], v[206:209], v[202:205], v[142:145]
	s_setprio 0
	s_nop 0
	ds_read_b128 v[150:153], v130 offset:45056
	ds_read_b128 v[162:165], v130 offset:47104
	v_cvt_pk_f16_f32 v39, v38, v39
	v_cvt_pk_f16_f32 v38, v36, v37
	ds_write_b64 v100, v[38:39] offset:28672
	s_setprio 1
	s_waitcnt lgkmcnt(1)
	v_mfma_f32_16x16x32_f16 v[36:39], v[150:153], v[182:185], v[48:51]
	v_mfma_f32_16x16x32_f16 v[48:51], v[150:153], v[186:189], v[76:79]
	v_mfma_f32_16x16x32_f16 v[76:79], v[150:153], v[190:193], v[158:161]
	v_mfma_f32_16x16x32_f16 v[150:153], v[150:153], v[202:205], v[154:157]
	v_mfma_f32_16x16x32_f16 v[154:157], v[162:165], v[182:185], v[166:169]
	v_mfma_f32_16x16x32_f16 v[158:161], v[162:165], v[186:189], v[174:177]
	v_mfma_f32_16x16x32_f16 v[166:169], v[162:165], v[190:193], v[178:181]
	v_mfma_f32_16x16x32_f16 v[162:165], v[162:165], v[202:205], v[170:173]
	s_setprio 0
	s_waitcnt vmcnt(0)
	s_waitcnt lgkmcnt(0)
	s_barrier
	s_nop 0
	ds_read_b128 v[170:173], v131
	ds_read_b128 v[174:177], v131 offset:2048
	ds_read_b128 v[178:181], v131 offset:4096
	ds_read_b128 v[182:185], v131 offset:6144
	ds_read_b128 v[186:189], v129
	ds_read_b128 v[190:193], v129 offset:2048
	v_lshl_add_u64 v[126:127], s[56:57], 0, v[196:197]
	s_mov_b32 m0, s0
	v_cvt_pk_f16_f32 v3, v2, v3
	global_load_lds_dwordx4 v[126:127], off
	v_cvt_pk_f16_f32 v2, v0, v1
	ds_write_b64 v100, v[2:3] offset:32768
	s_setprio 1
	s_waitcnt lgkmcnt(1)
	v_mfma_f32_16x16x32_f16 v[0:3], v[186:189], v[170:173], v[8:11]
	v_mfma_f32_16x16x32_f16 v[8:11], v[186:189], v[174:177], v[52:55]
	v_mfma_f32_16x16x32_f16 v[52:55], v[186:189], v[178:181], v[80:83]
	v_mfma_f32_16x16x32_f16 v[80:83], v[186:189], v[182:185], v[92:95]
	v_mfma_f32_16x16x32_f16 v[92:95], v[190:193], v[170:173], v[102:105]
	v_mfma_f32_16x16x32_f16 v[102:105], v[190:193], v[174:177], v[106:109]
	v_mfma_f32_16x16x32_f16 v[106:109], v[190:193], v[178:181], v[110:113]
	v_mfma_f32_16x16x32_f16 v[110:113], v[190:193], v[182:185], v[114:117]
	s_setprio 0
	s_nop 1
	ds_read_b128 v[114:117], v129 offset:4096
	ds_read_b128 v[186:189], v129 offset:6144
	s_mov_b32 m0, s1
	v_lshl_add_u64 v[190:191], v[126:127], 0, s[58:59]
	global_load_lds_dwordx4 v[190:191], off
	v_cvt_pk_f16_f32 v7, v6, v7
	v_cvt_pk_f16_f32 v6, v4, v5
	ds_write_b64 v100, v[6:7] offset:36864
	s_setprio 1
	s_waitcnt lgkmcnt(1)
	v_mfma_f32_16x16x32_f16 v[190:193], v[114:117], v[170:173], v[40:43]
	v_mfma_f32_16x16x32_f16 v[56:59], v[114:117], v[174:177], v[56:59]
	v_mfma_f32_16x16x32_f16 v[64:67], v[114:117], v[178:181], v[64:67]
	v_mfma_f32_16x16x32_f16 v[68:71], v[114:117], v[182:185], v[68:71]
	v_mfma_f32_16x16x32_f16 v[84:87], v[186:189], v[170:173], v[84:87]
	v_mfma_f32_16x16x32_f16 v[96:99], v[186:189], v[174:177], v[96:99]
	v_mfma_f32_16x16x32_f16 v[114:117], v[186:189], v[178:181], v[118:121]
	v_mfma_f32_16x16x32_f16 v[118:121], v[186:189], v[182:185], v[122:125]
	s_setprio 0
	ds_read_b128 v[4:7], v129 offset:8192
	ds_read_b128 v[40:43], v129 offset:10240
	s_mov_b32 m0, s70
	v_lshl_add_u64 v[122:123], v[126:127], 0, s[60:61]
	global_load_lds_dwordx4 v[122:123], off
	v_cvt_pk_f16_f32 v15, v14, v15
	v_cvt_pk_f16_f32 v14, v12, v13
	ds_write_b64 v100, v[14:15] offset:40960
	s_setprio 1
	s_waitcnt lgkmcnt(1)
	v_mfma_f32_16x16x32_f16 v[122:125], v[4:7], v[170:173], v[44:47]
	v_mfma_f32_16x16x32_f16 v[88:91], v[4:7], v[182:185], v[88:91]
	v_mfma_f32_16x16x32_f16 v[134:137], v[40:43], v[170:173], v[134:137]
	v_mfma_f32_16x16x32_f16 v[146:149], v[40:43], v[178:181], v[146:149]
	v_mfma_f32_16x16x32_f16 v[186:189], v[4:7], v[174:177], v[60:63]
	v_mfma_f32_16x16x32_f16 v[202:205], v[4:7], v[178:181], v[72:75]
	v_mfma_f32_16x16x32_f16 v[138:141], v[40:43], v[174:177], v[138:141]
	v_mfma_f32_16x16x32_f16 v[142:145], v[40:43], v[182:185], v[142:145]
	s_setprio 0
	ds_read_b128 v[4:7], v129 offset:12288
	ds_read_b128 v[12:15], v129 offset:14336
	s_mov_b32 m0, s71
	v_lshl_add_u64 v[40:41], v[126:127], 0, s[62:63]
	global_load_lds_dwordx4 v[40:41], off
	v_cvt_pk_f16_f32 v19, v18, v19
	v_cvt_pk_f16_f32 v18, v16, v17
	ds_write_b64 v100, v[18:19] offset:45056
	s_setprio 1
	s_waitcnt lgkmcnt(1)
	v_mfma_f32_16x16x32_f16 v[206:209], v[4:7], v[170:173], v[36:39]
	v_mfma_f32_16x16x32_f16 v[210:213], v[4:7], v[174:177], v[48:51]
	v_mfma_f32_16x16x32_f16 v[214:217], v[4:7], v[178:181], v[76:79]
	v_mfma_f32_16x16x32_f16 v[150:153], v[4:7], v[182:185], v[150:153]
	v_mfma_f32_16x16x32_f16 v[154:157], v[12:15], v[170:173], v[154:157]
	v_mfma_f32_16x16x32_f16 v[158:161], v[12:15], v[174:177], v[158:161]
	v_mfma_f32_16x16x32_f16 v[166:169], v[12:15], v[178:181], v[166:169]
	v_mfma_f32_16x16x32_f16 v[162:165], v[12:15], v[182:185], v[162:165]
	s_setprio 0
	ds_read_b128 v[170:173], v128
	ds_read_b128 v[174:177], v128 offset:2048
	ds_read_b128 v[178:181], v128 offset:4096
	ds_read_b128 v[182:185], v128 offset:6144
	ds_read_b128 v[12:15], v130
	ds_read_b128 v[40:43], v130 offset:2048
	v_cvt_pk_f16_f32 v5, v22, v23
	v_cvt_pk_f16_f32 v4, v20, v21
	ds_write_b64 v100, v[4:5] offset:49152
	s_setprio 1
	s_waitcnt lgkmcnt(1)
	v_mfma_f32_16x16x32_f16 v[0:3], v[12:15], v[170:173], v[0:3]
	v_mfma_f32_16x16x32_f16 v[4:7], v[12:15], v[174:177], v[8:11]
	v_mfma_f32_16x16x32_f16 v[8:11], v[12:15], v[178:181], v[52:55]
	v_mfma_f32_16x16x32_f16 v[12:15], v[12:15], v[182:185], v[80:83]
	v_mfma_f32_16x16x32_f16 v[16:19], v[40:43], v[170:173], v[92:95]
	v_mfma_f32_16x16x32_f16 v[20:23], v[40:43], v[174:177], v[102:105]
	v_mfma_f32_16x16x32_f16 v[36:39], v[40:43], v[178:181], v[106:109]
	v_mfma_f32_16x16x32_f16 v[40:43], v[40:43], v[182:185], v[110:113]
	s_setprio 0
	ds_read_b128 v[52:55], v130 offset:4096
	ds_read_b128 v[72:75], v130 offset:6144
	v_cvt_pk_f16_f32 v27, v26, v27
	v_cvt_pk_f16_f32 v26, v24, v25
	ds_write_b64 v100, v[26:27] offset:53248
	s_setprio 1
	s_waitcnt lgkmcnt(1)
	v_mfma_f32_16x16x32_f16 v[24:27], v[52:55], v[170:173], v[190:193]
	v_mfma_f32_16x16x32_f16 v[44:47], v[52:55], v[174:177], v[56:59]
	v_mfma_f32_16x16x32_f16 v[48:51], v[52:55], v[178:181], v[64:67]
	v_mfma_f32_16x16x32_f16 v[52:55], v[52:55], v[182:185], v[68:71]
	v_mfma_f32_16x16x32_f16 v[56:59], v[72:75], v[170:173], v[84:87]
	v_mfma_f32_16x16x32_f16 v[60:63], v[72:75], v[174:177], v[96:99]
	v_mfma_f32_16x16x32_f16 v[64:67], v[72:75], v[178:181], v[114:117]
	v_mfma_f32_16x16x32_f16 v[68:71], v[72:75], v[182:185], v[118:121]
	s_setprio 0
	ds_read_b128 v[80:83], v130 offset:8192
	ds_read_b128 v[96:99], v130 offset:10240
	v_cvt_pk_f16_f32 v31, v30, v31
	v_cvt_pk_f16_f32 v30, v28, v29
	ds_write_b64 v100, v[30:31] offset:57344
	s_setprio 1
	s_waitcnt lgkmcnt(1)
	v_mfma_f32_16x16x32_f16 v[28:31], v[80:83], v[170:173], v[122:125]
	v_mfma_f32_16x16x32_f16 v[72:75], v[80:83], v[174:177], v[186:189]
	v_mfma_f32_16x16x32_f16 v[76:79], v[80:83], v[178:181], v[202:205]
	v_mfma_f32_16x16x32_f16 v[80:83], v[80:83], v[182:185], v[88:91]
	v_mfma_f32_16x16x32_f16 v[84:87], v[96:99], v[170:173], v[134:137]
	v_mfma_f32_16x16x32_f16 v[88:91], v[96:99], v[174:177], v[138:141]
	v_mfma_f32_16x16x32_f16 v[92:95], v[96:99], v[178:181], v[146:149]
	v_mfma_f32_16x16x32_f16 v[96:99], v[96:99], v[182:185], v[142:145]
	s_setprio 0
	ds_read_b128 v[108:111], v130 offset:12288
	ds_read_b128 v[124:127], v130 offset:14336
	v_cvt_pk_f16_f32 v35, v34, v35
	v_cvt_pk_f16_f32 v34, v32, v33
	ds_write_b64 v100, v[34:35] offset:61440
	s_setprio 1
	s_waitcnt lgkmcnt(1)
	v_mfma_f32_16x16x32_f16 v[32:35], v[108:111], v[170:173], v[206:209]
	v_mfma_f32_16x16x32_f16 v[100:103], v[108:111], v[174:177], v[210:213]
	v_mfma_f32_16x16x32_f16 v[104:107], v[108:111], v[178:181], v[214:217]
	v_mfma_f32_16x16x32_f16 v[108:111], v[108:111], v[182:185], v[150:153]
	v_mfma_f32_16x16x32_f16 v[112:115], v[124:127], v[170:173], v[154:157]
	v_mfma_f32_16x16x32_f16 v[116:119], v[124:127], v[174:177], v[158:161]
	v_mfma_f32_16x16x32_f16 v[120:123], v[124:127], v[178:181], v[166:169]
	v_mfma_f32_16x16x32_f16 v[124:127], v[124:127], v[182:185], v[162:165]
	s_setprio 0
	s_waitcnt vmcnt(0)
	s_waitcnt lgkmcnt(0)
	s_barrier
	v_and_b32_e32 v133, 0x7ffffc00, v194
	v_add_u32_e32 v138, 0x2000, v133
	v_readfirstlane_b32 s0, v133
	v_lshl_add_u64 v[134:135], s[10:11], 0, v[196:197]
	s_mov_b32 m0, s0
	v_readfirstlane_b32 s0, v138
	v_add_u32_e32 v138, 0x4000, v133
	global_load_lds_dwordx4 v[134:135], off
	v_lshl_add_u64 v[136:137], v[134:135], 0, s[58:59]
	s_mov_b32 m0, s0
	v_readfirstlane_b32 s0, v138
	v_add_u32_e32 v138, 0x6000, v133
	global_load_lds_dwordx4 v[136:137], off
	v_lshl_add_u64 v[136:137], v[134:135], 0, s[60:61]
	s_mov_b32 m0, s0
	v_readfirstlane_b32 s0, v138
	global_load_lds_dwordx4 v[136:137], off
	v_lshl_add_u64 v[136:137], v[134:135], 0, s[62:63]
	s_mov_b32 m0, s0
	s_mov_b64 s[0:1], 0x8000
	v_add_u32_e32 v138, 0x10000, v133
	global_load_lds_dwordx4 v[136:137], off
	v_lshl_add_u64 v[136:137], v[134:135], 0, s[0:1]
	v_readfirstlane_b32 s0, v138
	s_mov_b32 m0, s0
	s_mov_b64 s[0:1], 0xa000
	v_add_u32_e32 v138, 0x12000, v133
	global_load_lds_dwordx4 v[136:137], off
	v_lshl_add_u64 v[136:137], v[134:135], 0, s[0:1]
	v_readfirstlane_b32 s0, v138
	v_add_u32_e32 v138, 0x14000, v133
	s_mov_b32 m0, s0
	v_readfirstlane_b32 s0, v138
	v_add_u32_e32 v133, 0x16000, v133
	global_load_lds_dwordx4 v[136:137], off
	v_lshl_add_u64 v[136:137], v[134:135], 0, s[66:67]
	s_mov_b32 m0, s0
	v_readfirstlane_b32 s0, v133
	global_load_lds_dwordx4 v[136:137], off
	v_lshl_add_u64 v[134:135], v[134:135], 0, s[68:69]
	s_mov_b32 m0, s0
	v_mov_b32_e32 v146, 0
	global_load_lds_dwordx4 v[134:135], off
	v_and_b32_e32 v134, 0xfffffff, v132
	v_cmp_gt_u32_e32 vcc, s82, v134
	v_mov_b32_e32 v132, 0
	v_mov_b32_e32 v133, 0
	s_and_saveexec_b64 s[0:1], vcc
	s_cbranch_execz .LBB1_7
	s_and_b32 s64, s78, 0x7ffffc00
	s_or_b32 s64, s64, s33
	v_or_b32_e32 v132, s64, v134
	v_mov_b32_e32 v133, v195
	v_lshl_add_u64 v[132:133], v[132:133], 2, s[12:13]
	global_load_dword v133, v[132:133], off
	v_or_b32_e32 v132, s33, v134
	v_lshlrev_b32_e32 v132, 2, v132
	global_load_dword v146, v132, s[16:17]
	s_nop 0
	global_load_dword v132, v132, s[14:15]
